# next-layer weight conversion moved into the shadow of 6 grid barriers per layer (waves 1..7, 3 tiles each); dedicated conversion loops removed
# baseline (speedup 1.0000x reference)
.LBB0_224:
	s_or_b64 exec, exec, s[0:1]
	v_readlane_b32 s12, v254, 1
	v_readlane_b32 s13, v254, 2
	v_readlane_b32 s69, v254, 41
	s_nop 3
	s_cmp_eq_u32 s69, 0
	s_cbranch_scc1 .Lcvb0_skip
	s_waitcnt vmcnt(0) lgkmcnt(0)
	v_readlane_b32 s0, v254, 42
	v_readlane_b32 s1, v254, 43
	v_readlane_b32 s60, v254, 0
	v_readlane_b32 s61, v254, 41
	s_nop 3
	s_sub_u32 s0, s0, 0xd0
	s_subb_u32 s1, s1, 0
	s_load_dwordx2 s[94:95], s[0:1], 0x20
	s_load_dwordx2 s[98:99], s[0:1], 0x28
	s_load_dwordx2 s[56:57], s[0:1], 0x88
	s_load_dwordx2 s[82:83], s[0:1], 0x90
	s_load_dwordx2 s[38:39], s[0:1], 0x98
	s_load_dwordx2 s[44:45], s[0:1], 0xa0
	s_load_dwordx2 s[46:47], s[0:1], 0xa8
	s_load_dwordx2 s[48:49], s[0:1], 0xb8
	v_mbcnt_lo_u32_b32 v100, -1, 0
	v_mbcnt_hi_u32_b32 v100, -1, v100
	v_and_b32_e32 v96, 7, v100
	v_lshrrev_b32_e32 v97, 3, v100
	v_mov_b32_e32 v98, 0x43e00000
	s_mov_b32 s64, 0xc3e00000
	s_mul_i32 s32, s60, 7
	s_add_u32 s32, s32, s61
	s_sub_u32 s32, s32, 1
	s_mul_i32 s32, s32, 3
	s_waitcnt lgkmcnt(0)
	s_add_u32 s56, s56, 0x4000000
	s_addc_u32 s57, s57, 0
	s_add_u32 s82, s82, 0x4000000
	s_addc_u32 s83, s83, 0
	s_add_u32 s38, s38, 0x4000000
	s_addc_u32 s39, s39, 0
	s_add_u32 s44, s44, 0x400000
	s_addc_u32 s45, s45, 0
	s_add_u32 s46, s46, 0x100000
	s_addc_u32 s47, s47, 0
	s_add_u32 s48, s48, 0x2bd00000
	s_addc_u32 s49, s49, 0
	s_mov_b32 s41, 0
	s_add_u32 s43, s32, 0
	s_cmp_lt_u32 s43, 0x6780
	s_cbranch_scc0 .Lcvb0_wait
	s_add_u32 s43, s32, 0
	s_cmp_lt_u32 s43, 0x300
	s_cbranch_scc0 .Lcvb0_d0_b
	s_mul_i32 s58, s43, 0xaaab
	s_lshr_b32 s58, s58, 21
	s_mul_i32 s59, s58, 48
	s_sub_u32 s59, s43, s59
	s_mul_i32 s60, s58, 0x60000
	s_mul_i32 s81, s59, 0x80
	s_add_u32 s60, s60, s81
	s_add_u32 s92, s94, s60
	s_addc_u32 s93, s95, 0
	s_mov_b32 s63, 0x1800
	s_mul_i32 s61, s59, 0x8000
	s_mul_i32 s81, s58, 0x40
	s_add_u32 s61, s61, s81
	s_add_u32 s61, s61, 0x800000
	s_add_u32 s50, s48, s61
	s_addc_u32 s51, s49, 0
	s_mov_b32 s65, 0x400
	s_mov_b32 s71, 0x44000000
	s_branch .Lcvb0_d0_ld
.Lcvb0_d0_b:
	s_sub_u32 s43, s43, 0x300
	s_cmp_lt_u32 s43, 0x200
	s_cbranch_scc0 .Lcvb0_d0_c
	s_lshr_b32 s58, s43, 5
	s_and_b32 s59, s43, 31
	s_mul_i32 s60, s58, 0x40000
	s_mul_i32 s81, s59, 0x80
	s_add_u32 s60, s60, s81
	s_add_u32 s92, s98, s60
	s_addc_u32 s93, s99, 0
	s_mov_b32 s63, 0x1000
	s_mul_i32 s61, s59, 0x8000
	s_mul_i32 s81, s58, 0x40
	s_add_u32 s61, s61, s81
	s_add_u32 s61, s61, 0xe00000
	s_add_u32 s50, s48, s61
	s_addc_u32 s51, s49, 0
	s_mov_b32 s65, 0x400
	s_mov_b32 s71, 0x44800000
	s_branch .Lcvb0_d0_ld
.Lcvb0_d0_c:
	s_sub_u32 s43, s43, 0x200
	s_cmp_lt_u32 s43, 0x2000
	s_cbranch_scc0 .Lcvb0_d0_dd
	s_lshr_b32 s80, s43, 8
	s_and_b32 s59, s43, 15
	s_bfe_u32 s58, s43, 0x40004
	s_lshr_b32 s81, s59, 2
	s_mul_i32 s61, s81, 0x40000
	s_and_b32 s81, s59, 3
	s_mul_i32 s81, s81, 0x8000
	s_add_u32 s61, s61, s81
	s_mul_i32 s81, s80, 0x100000
	s_add_u32 s61, s61, s81
	s_lshl_b32 s81, s58, 6
	s_add_u32 s61, s61, s81
	s_add_u32 s61, s61, 0x1000000
	s_add_u32 s50, s48, s61
	s_addc_u32 s51, s49, 0
	s_mul_i32 s60, s80, 0x200000
	s_mul_i32 s81, s58, 0x20000
	s_add_u32 s60, s60, s81
	s_lshl_b32 s81, s59, 7
	s_add_u32 s60, s60, s81
	s_add_u32 s92, s56, s60
	s_addc_u32 s93, s57, 0
	s_mov_b32 s63, 0x800
	s_mov_b32 s65, 0x400
	s_mov_b32 s71, 0x44000000
	s_branch .Lcvb0_d0_ld
.Lcvb0_d0_dd:
	s_sub_u32 s43, s43, 0x2000
	s_cmp_lt_u32 s43, 0x2000
	s_cbranch_scc0 .Lcvb0_d0_e
	s_lshr_b32 s80, s43, 8
	s_and_b32 s59, s43, 15
	s_bfe_u32 s58, s43, 0x40004
	s_lshr_b32 s81, s59, 2
	s_mul_i32 s61, s81, 0x40000
	s_and_b32 s81, s59, 3
	s_mul_i32 s81, s81, 0x8000
	s_add_u32 s61, s61, s81
	s_mul_i32 s81, s80, 0x100000
	s_add_u32 s61, s61, s81
	s_lshl_b32 s81, s58, 6
	s_add_u32 s61, s61, s81
	s_add_u32 s61, s61, 0x1020000
	s_add_u32 s50, s48, s61
	s_addc_u32 s51, s49, 0
	s_mul_i32 s60, s80, 0x200000
	s_mul_i32 s81, s58, 0x20000
	s_add_u32 s60, s60, s81
	s_lshl_b32 s81, s59, 7
	s_add_u32 s60, s60, s81
	s_add_u32 s92, s82, s60
	s_addc_u32 s93, s83, 0
	s_mov_b32 s63, 0x800
	s_mov_b32 s65, 0x400
	s_mov_b32 s71, 0x44000000
	s_branch .Lcvb0_d0_ld
.Lcvb0_d0_e:
	s_sub_u32 s43, s43, 0x2000
	s_cmp_lt_u32 s43, 0x2000
	s_cbranch_scc0 .Lcvb0_d0_f
	s_lshr_b32 s80, s43, 8
	s_and_b32 s59, s43, 31
	s_bfe_u32 s58, s43, 0x30005
	s_mul_i32 s60, s80, 0x200000
	s_mul_i32 s81, s58, 0x40000
	s_add_u32 s60, s60, s81
	s_mul_i32 s81, s59, 0x80
	s_add_u32 s60, s60, s81
	s_add_u32 s92, s38, s60
	s_addc_u32 s93, s39, 0
	s_mov_b32 s63, 0x1000
	s_mul_i32 s61, s80, 0x80000
	s_mul_i32 s81, s59, 0x4000
	s_add_u32 s61, s61, s81
	s_mul_i32 s81, s58, 0x40
	s_add_u32 s61, s61, s81
	s_add_u32 s61, s61, 0x5000000
	s_add_u32 s50, s48, s61
	s_addc_u32 s51, s49, 0
	s_mov_b32 s65, 0x200
	s_mov_b32 s71, 0x44800000
	s_branch .Lcvb0_d0_ld
.Lcvb0_d0_f:
	s_sub_u32 s43, s43, 0x2000
	s_cmp_lt_u32 s43, 0x200
	s_cbranch_scc0 .Lcvb0_d0_g
	s_lshr_b32 s58, s43, 5
	s_and_b32 s59, s43, 31
	s_mul_i32 s60, s58, 0x40000
	s_mul_i32 s81, s59, 0x80
	s_add_u32 s60, s60, s81
	s_add_u32 s92, s44, s60
	s_addc_u32 s93, s45, 0
	s_mov_b32 s63, 0x1000
	s_mul_i32 s61, s59, 0x10000
	s_mul_i32 s81, s58, 0x80
	s_add_u32 s61, s61, s81
	s_add_u32 s61, s61, 0x7000000
	s_add_u32 s50, s48, s61
	s_addc_u32 s51, s49, 0
	s_mov_b32 s65, 0x800
	s_mov_b32 s71, 0x0
	s_branch .Lcvb0_d0_ld
.Lcvb0_d0_g:
	s_sub_u32 s43, s43, 0x200
	s_lshr_b32 s58, s43, 5
	s_and_b32 s59, s43, 31
	s_mul_i32 s60, s58, 0x40000
	s_mul_i32 s81, s59, 0x80
	s_add_u32 s60, s60, s81
	s_add_u32 s92, s46, s60
	s_addc_u32 s93, s47, 0
	s_mov_b32 s63, 0x1000
	s_mul_i32 s61, s59, 0x4000
	s_mul_i32 s81, s58, 0x80
	s_add_u32 s61, s61, s81
	s_add_u32 s61, s61, 0x7200000
	s_add_u32 s50, s48, s61
	s_addc_u32 s51, s49, 0
	s_mov_b32 s65, 0x200
	s_mov_b32 s71, 0x0
	s_branch .Lcvb0_d0_ld
.Lcvb0_d0_ld:
	s_lshl_b32 s60, s63, 3
	v_mul_lo_u32 v0, v96, s60
	v_lshl_add_u32 v0, v97, 4, v0
	v_add_u32_e32 v4, s63, v0
	v_add_u32_e32 v10, s63, v4
	v_add_u32_e32 v11, s63, v10
	v_add_u32_e32 v12, s63, v11
	v_add_u32_e32 v19, s63, v12
	v_add_u32_e32 v24, s63, v19
	v_add_u32_e32 v25, s63, v24
	global_load_dwordx4 v[34:37], v0, s[92:93] nt
	global_load_dwordx4 v[38:41], v4, s[92:93] nt
	global_load_dwordx4 v[42:45], v10, s[92:93] nt
	global_load_dwordx4 v[46:49], v11, s[92:93] nt
	global_load_dwordx4 v[50:53], v12, s[92:93] nt
	global_load_dwordx4 v[54:57], v19, s[92:93] nt
	global_load_dwordx4 v[58:61], v24, s[92:93] nt
	global_load_dwordx4 v[62:65], v25, s[92:93] nt
	s_mov_b32 s41, 1
	s_add_u32 s43, s32, 1
	s_cmp_lt_u32 s43, 0x6780
	s_cbranch_scc0 .Lcvb0_wait
	s_add_u32 s43, s32, 1
	s_cmp_lt_u32 s43, 0x300
	s_cbranch_scc0 .Lcvb0_d1_b
	s_mul_i32 s58, s43, 0xaaab
	s_lshr_b32 s58, s58, 21
	s_mul_i32 s59, s58, 48
	s_sub_u32 s59, s43, s59
	s_mul_i32 s60, s58, 0x60000
	s_mul_i32 s81, s59, 0x80
	s_add_u32 s60, s60, s81
	s_add_u32 s92, s94, s60
	s_addc_u32 s93, s95, 0
	s_mov_b32 s63, 0x1800
	s_mul_i32 s61, s59, 0x8000
	s_mul_i32 s81, s58, 0x40
	s_add_u32 s61, s61, s81
	s_add_u32 s61, s61, 0x800000
	s_add_u32 s52, s48, s61
	s_addc_u32 s53, s49, 0
	s_mov_b32 s66, 0x400
	s_mov_b32 s75, 0x44000000
	s_branch .Lcvb0_d1_ld
.Lcvb0_d1_b:
	s_sub_u32 s43, s43, 0x300
	s_cmp_lt_u32 s43, 0x200
	s_cbranch_scc0 .Lcvb0_d1_c
	s_lshr_b32 s58, s43, 5
	s_and_b32 s59, s43, 31
	s_mul_i32 s60, s58, 0x40000
	s_mul_i32 s81, s59, 0x80
	s_add_u32 s60, s60, s81
	s_add_u32 s92, s98, s60
	s_addc_u32 s93, s99, 0
	s_mov_b32 s63, 0x1000
	s_mul_i32 s61, s59, 0x8000
	s_mul_i32 s81, s58, 0x40
	s_add_u32 s61, s61, s81
	s_add_u32 s61, s61, 0xe00000
	s_add_u32 s52, s48, s61
	s_addc_u32 s53, s49, 0
	s_mov_b32 s66, 0x400
	s_mov_b32 s75, 0x44800000
	s_branch .Lcvb0_d1_ld
.Lcvb0_d1_c:
	s_sub_u32 s43, s43, 0x200
	s_cmp_lt_u32 s43, 0x2000
	s_cbranch_scc0 .Lcvb0_d1_dd
	s_lshr_b32 s80, s43, 8
	s_and_b32 s59, s43, 15
	s_bfe_u32 s58, s43, 0x40004
	s_lshr_b32 s81, s59, 2
	s_mul_i32 s61, s81, 0x40000
	s_and_b32 s81, s59, 3
	s_mul_i32 s81, s81, 0x8000
	s_add_u32 s61, s61, s81
	s_mul_i32 s81, s80, 0x100000
	s_add_u32 s61, s61, s81
	s_lshl_b32 s81, s58, 6
	s_add_u32 s61, s61, s81
	s_add_u32 s61, s61, 0x1000000
	s_add_u32 s52, s48, s61
	s_addc_u32 s53, s49, 0
	s_mul_i32 s60, s80, 0x200000
	s_mul_i32 s81, s58, 0x20000
	s_add_u32 s60, s60, s81
	s_lshl_b32 s81, s59, 7
	s_add_u32 s60, s60, s81
	s_add_u32 s92, s56, s60
	s_addc_u32 s93, s57, 0
	s_mov_b32 s63, 0x800
	s_mov_b32 s66, 0x400
	s_mov_b32 s75, 0x44000000
	s_branch .Lcvb0_d1_ld
.Lcvb0_d1_dd:
	s_sub_u32 s43, s43, 0x2000
	s_cmp_lt_u32 s43, 0x2000
	s_cbranch_scc0 .Lcvb0_d1_e
	s_lshr_b32 s80, s43, 8
	s_and_b32 s59, s43, 15
	s_bfe_u32 s58, s43, 0x40004
	s_lshr_b32 s81, s59, 2
	s_mul_i32 s61, s81, 0x40000
	s_and_b32 s81, s59, 3
	s_mul_i32 s81, s81, 0x8000
	s_add_u32 s61, s61, s81
	s_mul_i32 s81, s80, 0x100000
	s_add_u32 s61, s61, s81
	s_lshl_b32 s81, s58, 6
	s_add_u32 s61, s61, s81
	s_add_u32 s61, s61, 0x1020000
	s_add_u32 s52, s48, s61
	s_addc_u32 s53, s49, 0
	s_mul_i32 s60, s80, 0x200000
	s_mul_i32 s81, s58, 0x20000
	s_add_u32 s60, s60, s81
	s_lshl_b32 s81, s59, 7
	s_add_u32 s60, s60, s81
	s_add_u32 s92, s82, s60
	s_addc_u32 s93, s83, 0
	s_mov_b32 s63, 0x800
	s_mov_b32 s66, 0x400
	s_mov_b32 s75, 0x44000000
	s_branch .Lcvb0_d1_ld
.Lcvb0_d1_e:
	s_sub_u32 s43, s43, 0x2000
	s_cmp_lt_u32 s43, 0x2000
	s_cbranch_scc0 .Lcvb0_d1_f
	s_lshr_b32 s80, s43, 8
	s_and_b32 s59, s43, 31
	s_bfe_u32 s58, s43, 0x30005
	s_mul_i32 s60, s80, 0x200000
	s_mul_i32 s81, s58, 0x40000
	s_add_u32 s60, s60, s81
	s_mul_i32 s81, s59, 0x80
	s_add_u32 s60, s60, s81
	s_add_u32 s92, s38, s60
	s_addc_u32 s93, s39, 0
	s_mov_b32 s63, 0x1000
	s_mul_i32 s61, s80, 0x80000
	s_mul_i32 s81, s59, 0x4000
	s_add_u32 s61, s61, s81
	s_mul_i32 s81, s58, 0x40
	s_add_u32 s61, s61, s81
	s_add_u32 s61, s61, 0x5000000
	s_add_u32 s52, s48, s61
	s_addc_u32 s53, s49, 0
	s_mov_b32 s66, 0x200
	s_mov_b32 s75, 0x44800000
	s_branch .Lcvb0_d1_ld
.Lcvb0_d1_f:
	s_sub_u32 s43, s43, 0x2000
	s_cmp_lt_u32 s43, 0x200
	s_cbranch_scc0 .Lcvb0_d1_g
	s_lshr_b32 s58, s43, 5
	s_and_b32 s59, s43, 31
	s_mul_i32 s60, s58, 0x40000
	s_mul_i32 s81, s59, 0x80
	s_add_u32 s60, s60, s81
	s_add_u32 s92, s44, s60
	s_addc_u32 s93, s45, 0
	s_mov_b32 s63, 0x1000
	s_mul_i32 s61, s59, 0x10000
	s_mul_i32 s81, s58, 0x80
	s_add_u32 s61, s61, s81
	s_add_u32 s61, s61, 0x7000000
	s_add_u32 s52, s48, s61
	s_addc_u32 s53, s49, 0
	s_mov_b32 s66, 0x800
	s_mov_b32 s75, 0x0
	s_branch .Lcvb0_d1_ld
.Lcvb0_d1_g:
	s_sub_u32 s43, s43, 0x200
	s_lshr_b32 s58, s43, 5
	s_and_b32 s59, s43, 31
	s_mul_i32 s60, s58, 0x40000
	s_mul_i32 s81, s59, 0x80
	s_add_u32 s60, s60, s81
	s_add_u32 s92, s46, s60
	s_addc_u32 s93, s47, 0
	s_mov_b32 s63, 0x1000
	s_mul_i32 s61, s59, 0x4000
	s_mul_i32 s81, s58, 0x80
	s_add_u32 s61, s61, s81
	s_add_u32 s61, s61, 0x7200000
	s_add_u32 s52, s48, s61
	s_addc_u32 s53, s49, 0
	s_mov_b32 s66, 0x200
	s_mov_b32 s75, 0x0
	s_branch .Lcvb0_d1_ld
.Lcvb0_d1_ld:
	s_lshl_b32 s60, s63, 3
	v_mul_lo_u32 v0, v96, s60
	v_lshl_add_u32 v0, v97, 4, v0
	v_add_u32_e32 v4, s63, v0
	v_add_u32_e32 v10, s63, v4
	v_add_u32_e32 v11, s63, v10
	v_add_u32_e32 v12, s63, v11
	v_add_u32_e32 v19, s63, v12
	v_add_u32_e32 v24, s63, v19
	v_add_u32_e32 v25, s63, v24
	global_load_dwordx4 v[66:69], v0, s[92:93] nt
	global_load_dwordx4 v[70:73], v4, s[92:93] nt
	global_load_dwordx4 v[74:77], v10, s[92:93] nt
	global_load_dwordx4 v[78:81], v11, s[92:93] nt
	global_load_dwordx4 v[82:85], v12, s[92:93] nt
	global_load_dwordx4 v[86:89], v19, s[92:93] nt
	global_load_dwordx4 v[102:105], v24, s[92:93] nt
	global_load_dwordx4 v[106:109], v25, s[92:93] nt
	s_mov_b32 s41, 2
	s_add_u32 s43, s32, 2
	s_cmp_lt_u32 s43, 0x6780
	s_cbranch_scc0 .Lcvb0_wait
	s_add_u32 s43, s32, 2
	s_cmp_lt_u32 s43, 0x300
	s_cbranch_scc0 .Lcvb0_d2_b
	s_mul_i32 s58, s43, 0xaaab
	s_lshr_b32 s58, s58, 21
	s_mul_i32 s59, s58, 48
	s_sub_u32 s59, s43, s59
	s_mul_i32 s60, s58, 0x60000
	s_mul_i32 s81, s59, 0x80
	s_add_u32 s60, s60, s81
	s_add_u32 s92, s94, s60
	s_addc_u32 s93, s95, 0
	s_mov_b32 s63, 0x1800
	s_mul_i32 s61, s59, 0x8000
	s_mul_i32 s81, s58, 0x40
	s_add_u32 s61, s61, s81
	s_add_u32 s61, s61, 0x800000
	s_add_u32 s54, s48, s61
	s_addc_u32 s55, s49, 0
	s_mov_b32 s67, 0x400
	s_mov_b32 s78, 0x44000000
	s_branch .Lcvb0_d2_ld
.Lcvb0_d2_b:
	s_sub_u32 s43, s43, 0x300
	s_cmp_lt_u32 s43, 0x200
	s_cbranch_scc0 .Lcvb0_d2_c
	s_lshr_b32 s58, s43, 5
	s_and_b32 s59, s43, 31
	s_mul_i32 s60, s58, 0x40000
	s_mul_i32 s81, s59, 0x80
	s_add_u32 s60, s60, s81
	s_add_u32 s92, s98, s60
	s_addc_u32 s93, s99, 0
	s_mov_b32 s63, 0x1000
	s_mul_i32 s61, s59, 0x8000
	s_mul_i32 s81, s58, 0x40
	s_add_u32 s61, s61, s81
	s_add_u32 s61, s61, 0xe00000
	s_add_u32 s54, s48, s61
	s_addc_u32 s55, s49, 0
	s_mov_b32 s67, 0x400
	s_mov_b32 s78, 0x44800000
	s_branch .Lcvb0_d2_ld
.Lcvb0_d2_c:
	s_sub_u32 s43, s43, 0x200
	s_cmp_lt_u32 s43, 0x2000
	s_cbranch_scc0 .Lcvb0_d2_dd
	s_lshr_b32 s80, s43, 8
	s_and_b32 s59, s43, 15
	s_bfe_u32 s58, s43, 0x40004
	s_lshr_b32 s81, s59, 2
	s_mul_i32 s61, s81, 0x40000
	s_and_b32 s81, s59, 3
	s_mul_i32 s81, s81, 0x8000
	s_add_u32 s61, s61, s81
	s_mul_i32 s81, s80, 0x100000
	s_add_u32 s61, s61, s81
	s_lshl_b32 s81, s58, 6
	s_add_u32 s61, s61, s81
	s_add_u32 s61, s61, 0x1000000
	s_add_u32 s54, s48, s61
	s_addc_u32 s55, s49, 0
	s_mul_i32 s60, s80, 0x200000
	s_mul_i32 s81, s58, 0x20000
	s_add_u32 s60, s60, s81
	s_lshl_b32 s81, s59, 7
	s_add_u32 s60, s60, s81
	s_add_u32 s92, s56, s60
	s_addc_u32 s93, s57, 0
	s_mov_b32 s63, 0x800
	s_mov_b32 s67, 0x400
	s_mov_b32 s78, 0x44000000
	s_branch .Lcvb0_d2_ld
.Lcvb0_d2_dd:
	s_sub_u32 s43, s43, 0x2000
	s_cmp_lt_u32 s43, 0x2000
	s_cbranch_scc0 .Lcvb0_d2_e
	s_lshr_b32 s80, s43, 8
	s_and_b32 s59, s43, 15
	s_bfe_u32 s58, s43, 0x40004
	s_lshr_b32 s81, s59, 2
	s_mul_i32 s61, s81, 0x40000
	s_and_b32 s81, s59, 3
	s_mul_i32 s81, s81, 0x8000
	s_add_u32 s61, s61, s81
	s_mul_i32 s81, s80, 0x100000
	s_add_u32 s61, s61, s81
	s_lshl_b32 s81, s58, 6
	s_add_u32 s61, s61, s81
	s_add_u32 s61, s61, 0x1020000
	s_add_u32 s54, s48, s61
	s_addc_u32 s55, s49, 0
	s_mul_i32 s60, s80, 0x200000
	s_mul_i32 s81, s58, 0x20000
	s_add_u32 s60, s60, s81
	s_lshl_b32 s81, s59, 7
	s_add_u32 s60, s60, s81
	s_add_u32 s92, s82, s60
	s_addc_u32 s93, s83, 0
	s_mov_b32 s63, 0x800
	s_mov_b32 s67, 0x400
	s_mov_b32 s78, 0x44000000
	s_branch .Lcvb0_d2_ld
.Lcvb0_d2_e:
	s_sub_u32 s43, s43, 0x2000
	s_cmp_lt_u32 s43, 0x2000
	s_cbranch_scc0 .Lcvb0_d2_f
	s_lshr_b32 s80, s43, 8
	s_and_b32 s59, s43, 31
	s_bfe_u32 s58, s43, 0x30005
	s_mul_i32 s60, s80, 0x200000
	s_mul_i32 s81, s58, 0x40000
	s_add_u32 s60, s60, s81
	s_mul_i32 s81, s59, 0x80
	s_add_u32 s60, s60, s81
	s_add_u32 s92, s38, s60
	s_addc_u32 s93, s39, 0
	s_mov_b32 s63, 0x1000
	s_mul_i32 s61, s80, 0x80000
	s_mul_i32 s81, s59, 0x4000
	s_add_u32 s61, s61, s81
	s_mul_i32 s81, s58, 0x40
	s_add_u32 s61, s61, s81
	s_add_u32 s61, s61, 0x5000000
	s_add_u32 s54, s48, s61
	s_addc_u32 s55, s49, 0
	s_mov_b32 s67, 0x200
	s_mov_b32 s78, 0x44800000
	s_branch .Lcvb0_d2_ld
.Lcvb0_d2_f:
	s_sub_u32 s43, s43, 0x2000
	s_cmp_lt_u32 s43, 0x200
	s_cbranch_scc0 .Lcvb0_d2_g
	s_lshr_b32 s58, s43, 5
	s_and_b32 s59, s43, 31
	s_mul_i32 s60, s58, 0x40000
	s_mul_i32 s81, s59, 0x80
	s_add_u32 s60, s60, s81
	s_add_u32 s92, s44, s60
	s_addc_u32 s93, s45, 0
	s_mov_b32 s63, 0x1000
	s_mul_i32 s61, s59, 0x10000
	s_mul_i32 s81, s58, 0x80
	s_add_u32 s61, s61, s81
	s_add_u32 s61, s61, 0x7000000
	s_add_u32 s54, s48, s61
	s_addc_u32 s55, s49, 0
	s_mov_b32 s67, 0x800
	s_mov_b32 s78, 0x0
	s_branch .Lcvb0_d2_ld
.Lcvb0_d2_g:
	s_sub_u32 s43, s43, 0x200
	s_lshr_b32 s58, s43, 5
	s_and_b32 s59, s43, 31
	s_mul_i32 s60, s58, 0x40000
	s_mul_i32 s81, s59, 0x80
	s_add_u32 s60, s60, s81
	s_add_u32 s92, s46, s60
	s_addc_u32 s93, s47, 0
	s_mov_b32 s63, 0x1000
	s_mul_i32 s61, s59, 0x4000
	s_mul_i32 s81, s58, 0x80
	s_add_u32 s61, s61, s81
	s_add_u32 s61, s61, 0x7200000
	s_add_u32 s54, s48, s61
	s_addc_u32 s55, s49, 0
	s_mov_b32 s67, 0x200
	s_mov_b32 s78, 0x0
	s_branch .Lcvb0_d2_ld
.Lcvb0_d2_ld:
	s_lshl_b32 s60, s63, 3
	v_mul_lo_u32 v0, v96, s60
	v_lshl_add_u32 v0, v97, 4, v0
	v_add_u32_e32 v4, s63, v0
	v_add_u32_e32 v10, s63, v4
	v_add_u32_e32 v11, s63, v10
	v_add_u32_e32 v12, s63, v11
	v_add_u32_e32 v19, s63, v12
	v_add_u32_e32 v24, s63, v19
	v_add_u32_e32 v25, s63, v24
	global_load_dwordx4 v[110:113], v0, s[92:93] nt
	global_load_dwordx4 v[114:117], v4, s[92:93] nt
	global_load_dwordx4 v[118:121], v10, s[92:93] nt
	global_load_dwordx4 v[122:125], v11, s[92:93] nt
	global_load_dwordx4 v[126:129], v12, s[92:93] nt
	global_load_dwordx4 v[130:133], v19, s[92:93] nt
	global_load_dwordx4 v[134:137], v24, s[92:93] nt
	global_load_dwordx4 v[138:141], v25, s[92:93] nt
	s_mov_b32 s41, 3

.Lcvb0_p5_end:
.Lcvb0_fin:
	s_waitcnt vmcnt(0)
.Lcvb0_skip:
	s_waitcnt lgkmcnt(0)
	s_barrier
	v_readlane_b32 s14, v254, 3
	v_readlane_b32 s15, v254, 4

.LBB0_300:
	s_or_b64 exec, exec, s[0:1]
	v_readlane_b32 s12, v254, 1
	v_readlane_b32 s13, v254, 2
	v_readlane_b32 s69, v254, 41
	s_nop 3
	s_cmp_eq_u32 s69, 0
	s_cbranch_scc1 .Lcvb1_skip
	s_waitcnt vmcnt(0) lgkmcnt(0)
	v_readlane_b32 s0, v254, 42
	v_readlane_b32 s1, v254, 43
	v_readlane_b32 s60, v254, 0
	v_readlane_b32 s61, v254, 41
	s_nop 3
	s_sub_u32 s0, s0, 0xd0
	s_subb_u32 s1, s1, 0
	s_load_dwordx2 s[94:95], s[0:1], 0x20
	s_load_dwordx2 s[98:99], s[0:1], 0x28
	s_load_dwordx2 s[56:57], s[0:1], 0x88
	s_load_dwordx2 s[82:83], s[0:1], 0x90
	s_load_dwordx2 s[38:39], s[0:1], 0x98
	s_load_dwordx2 s[44:45], s[0:1], 0xa0
	s_load_dwordx2 s[46:47], s[0:1], 0xa8
	s_load_dwordx2 s[48:49], s[0:1], 0xb8
	v_mbcnt_lo_u32_b32 v100, -1, 0
	v_mbcnt_hi_u32_b32 v100, -1, v100
	v_and_b32_e32 v96, 7, v100
	v_lshrrev_b32_e32 v97, 3, v100
	v_mov_b32_e32 v98, 0x43e00000
	s_mov_b32 s64, 0xc3e00000
	s_mul_i32 s32, s60, 7
	s_add_u32 s32, s32, s61
	s_sub_u32 s32, s32, 1
	s_mul_i32 s43, s74, 7
	s_add_u32 s32, s32, s43
	s_mul_i32 s32, s32, 3
	s_waitcnt lgkmcnt(0)
	s_add_u32 s56, s56, 0x4000000
	s_addc_u32 s57, s57, 0
	s_add_u32 s82, s82, 0x4000000
	s_addc_u32 s83, s83, 0
	s_add_u32 s38, s38, 0x4000000
	s_addc_u32 s39, s39, 0
	s_add_u32 s44, s44, 0x400000
	s_addc_u32 s45, s45, 0
	s_add_u32 s46, s46, 0x100000
	s_addc_u32 s47, s47, 0
	s_add_u32 s48, s48, 0x2bd00000
	s_addc_u32 s49, s49, 0
	s_mov_b32 s41, 0
	s_add_u32 s43, s32, 0
	s_cmp_lt_u32 s43, 0x6780
	s_cbranch_scc0 .Lcvb1_wait
	s_add_u32 s43, s32, 0
	s_cmp_lt_u32 s43, 0x300
	s_cbranch_scc0 .Lcvb1_d0_b
	s_mul_i32 s58, s43, 0xaaab
	s_lshr_b32 s58, s58, 21
	s_mul_i32 s59, s58, 48
	s_sub_u32 s59, s43, s59
	s_mul_i32 s60, s58, 0x60000
	s_mul_i32 s81, s59, 0x80
	s_add_u32 s60, s60, s81
	s_add_u32 s92, s94, s60
	s_addc_u32 s93, s95, 0
	s_mov_b32 s63, 0x1800
	s_mul_i32 s61, s59, 0x8000
	s_mul_i32 s81, s58, 0x40
	s_add_u32 s61, s61, s81
	s_add_u32 s61, s61, 0x800000
	s_add_u32 s50, s48, s61
	s_addc_u32 s51, s49, 0
	s_mov_b32 s65, 0x400
	s_mov_b32 s71, 0x44000000
	s_branch .Lcvb1_d0_ld

.Lcvt_site_398:
	s_waitcnt vmcnt(0) lgkmcnt(0)
	v_readlane_b32 s0, v254, 42
	v_readlane_b32 s1, v254, 43
	v_readlane_b32 s60, v254, 0
	v_readlane_b32 s61, v254, 41
	s_nop 3
	s_sub_u32 s0, s0, 0xd0
	s_subb_u32 s1, s1, 0
	s_load_dwordx2 s[10:11], s[0:1], 0x20
	s_load_dwordx2 s[12:13], s[0:1], 0x28
	s_load_dwordx2 s[14:15], s[0:1], 0x88
	s_load_dwordx2 s[28:29], s[0:1], 0x90
	s_load_dwordx2 s[38:39], s[0:1], 0x98
	s_load_dwordx2 s[44:45], s[0:1], 0xa0
	s_load_dwordx2 s[46:47], s[0:1], 0xa8
	s_load_dwordx2 s[48:49], s[0:1], 0xb8
	v_mbcnt_lo_u32_b32 v100, -1, 0
	v_mbcnt_hi_u32_b32 v100, -1, v100
	v_and_b32_e32 v96, 7, v100
	v_lshrrev_b32_e32 v97, 3, v100
	v_mov_b32_e32 v98, 0x43e00000
	s_mov_b32 s64, 0xc3e00000
	s_lshl_b32 s9, s60, 3
	s_add_u32 s9, s9, s61
	s_min_u32 s20, s74, 0x40
	s_lshl_b32 s20, s20, 5
	s_waitcnt lgkmcnt(0)
	s_add_u32 s14, s14, 0x4000000
	s_addc_u32 s15, s15, 0
	s_add_u32 s28, s28, 0x4000000
	s_addc_u32 s29, s29, 0
	s_add_u32 s38, s38, 0x4000000
	s_addc_u32 s39, s39, 0
	s_add_u32 s44, s44, 0x400000
	s_addc_u32 s45, s45, 0
	s_add_u32 s46, s46, 0x100000
	s_addc_u32 s47, s47, 0
	s_add_u32 s48, s48, 0x2bd00000
	s_addc_u32 s49, s49, 0
	s_mul_i32 s32, s74, 126
	s_lshl_b32 s60, s9, 2
	s_add_u32 s32, s32, s60
	s_mov_b32 s41, 0
	s_cmp_lt_u32 s32, 0x6780
	s_cbranch_scc0 .Lcv398_drain0
	s_add_u32 s43, s32, 0
	s_cmp_lt_u32 s43, 0x300
	s_cbranch_scc0 .Lcv398_d0_b
	s_mul_i32 s58, s43, 0xaaab
	s_lshr_b32 s58, s58, 21
	s_mul_i32 s59, s58, 48
	s_sub_u32 s59, s43, s59
	s_mul_i32 s60, s58, 0x60000
	s_mul_i32 s81, s59, 0x80
	s_add_u32 s60, s60, s81
	s_add_u32 s2, s10, s60
	s_addc_u32 s3, s11, 0
	s_mov_b32 s63, 0x1800
	s_mul_i32 s61, s59, 0x8000
	s_mul_i32 s81, s58, 0x40
	s_add_u32 s61, s61, s81
	s_add_u32 s61, s61, 0x800000
	s_add_u32 s50, s48, s61
	s_addc_u32 s51, s49, 0
	s_mov_b32 s65, 0x400
	s_mov_b32 s71, 0x44000000
	s_branch .Lcv398_d0_ld

.LBB0_570:
	s_or_b64 exec, exec, s[0:1]
	v_readlane_b32 s12, v254, 1
	v_readlane_b32 s13, v254, 2
	v_readlane_b32 s69, v254, 41
	s_nop 3
	s_cmp_eq_u32 s69, 0
	s_cbranch_scc1 .Lcvb3_skip
	s_waitcnt vmcnt(0) lgkmcnt(0)
	v_readlane_b32 s0, v254, 42
	v_readlane_b32 s1, v254, 43
	v_readlane_b32 s60, v254, 0
	v_readlane_b32 s61, v254, 41
	s_nop 3
	s_sub_u32 s0, s0, 0xd0
	s_subb_u32 s1, s1, 0
	s_load_dwordx2 s[94:95], s[0:1], 0x20
	s_load_dwordx2 s[98:99], s[0:1], 0x28
	s_load_dwordx2 s[56:57], s[0:1], 0x88
	s_load_dwordx2 s[82:83], s[0:1], 0x90
	s_load_dwordx2 s[38:39], s[0:1], 0x98
	s_load_dwordx2 s[44:45], s[0:1], 0xa0
	s_load_dwordx2 s[46:47], s[0:1], 0xa8
	s_load_dwordx2 s[48:49], s[0:1], 0xb8
	v_mbcnt_lo_u32_b32 v100, -1, 0
	v_mbcnt_hi_u32_b32 v100, -1, v100
	v_and_b32_e32 v96, 7, v100
	v_lshrrev_b32_e32 v97, 3, v100
	v_mov_b32_e32 v98, 0x43e00000
	s_mov_b32 s64, 0xc3e00000
	s_mul_i32 s32, s60, 7
	s_add_u32 s32, s32, s61
	s_sub_u32 s32, s32, 1
	s_mul_i32 s43, s74, 14
	s_add_u32 s32, s32, s43
	s_mul_i32 s32, s32, 3
	s_waitcnt lgkmcnt(0)
	s_add_u32 s56, s56, 0x4000000
	s_addc_u32 s57, s57, 0
	s_add_u32 s82, s82, 0x4000000
	s_addc_u32 s83, s83, 0
	s_add_u32 s38, s38, 0x4000000
	s_addc_u32 s39, s39, 0
	s_add_u32 s44, s44, 0x400000
	s_addc_u32 s45, s45, 0
	s_add_u32 s46, s46, 0x100000
	s_addc_u32 s47, s47, 0
	s_add_u32 s48, s48, 0x2bd00000
	s_addc_u32 s49, s49, 0
	s_mov_b32 s41, 0
	s_add_u32 s43, s32, 0
	s_cmp_lt_u32 s43, 0x6780
	s_cbranch_scc0 .Lcvb3_wait
	s_add_u32 s43, s32, 0
	s_cmp_lt_u32 s43, 0x300
	s_cbranch_scc0 .Lcvb3_d0_b
	s_mul_i32 s58, s43, 0xaaab
	s_lshr_b32 s58, s58, 21
	s_mul_i32 s59, s58, 48
	s_sub_u32 s59, s43, s59
	s_mul_i32 s60, s58, 0x60000
	s_mul_i32 s81, s59, 0x80
	s_add_u32 s60, s60, s81
	s_add_u32 s92, s94, s60
	s_addc_u32 s93, s95, 0
	s_mov_b32 s63, 0x1800
	s_mul_i32 s61, s59, 0x8000
	s_mul_i32 s81, s58, 0x40
	s_add_u32 s61, s61, s81
	s_add_u32 s61, s61, 0x800000
	s_add_u32 s50, s48, s61
	s_addc_u32 s51, s49, 0
	s_mov_b32 s65, 0x400
	s_mov_b32 s71, 0x44000000
	s_branch .Lcvb3_d0_ld

.LBB0_724:
	s_or_b64 exec, exec, s[0:1]
	v_readlane_b32 s12, v254, 1
	v_readlane_b32 s13, v254, 2
	v_readlane_b32 s69, v254, 41
	s_nop 3
	s_cmp_eq_u32 s69, 0
	s_cbranch_scc1 .Lcvb4_skip
	s_waitcnt vmcnt(0) lgkmcnt(0)
	v_readlane_b32 s0, v254, 42
	v_readlane_b32 s1, v254, 43
	v_readlane_b32 s60, v254, 0
	v_readlane_b32 s61, v254, 41
	s_nop 3
	s_sub_u32 s0, s0, 0xd0
	s_subb_u32 s1, s1, 0
	s_load_dwordx2 s[94:95], s[0:1], 0x20
	s_load_dwordx2 s[98:99], s[0:1], 0x28
	s_load_dwordx2 s[56:57], s[0:1], 0x88
	s_load_dwordx2 s[82:83], s[0:1], 0x90
	s_load_dwordx2 s[38:39], s[0:1], 0x98
	s_load_dwordx2 s[44:45], s[0:1], 0xa0
	s_load_dwordx2 s[46:47], s[0:1], 0xa8
	s_load_dwordx2 s[48:49], s[0:1], 0xb8
	v_mbcnt_lo_u32_b32 v100, -1, 0
	v_mbcnt_hi_u32_b32 v100, -1, v100
	v_and_b32_e32 v96, 7, v100
	v_lshrrev_b32_e32 v97, 3, v100
	v_mov_b32_e32 v98, 0x43e00000
	s_mov_b32 s64, 0xc3e00000
	s_mul_i32 s32, s60, 7
	s_add_u32 s32, s32, s61
	s_sub_u32 s32, s32, 1
	s_mul_i32 s43, s74, 21
	s_add_u32 s32, s32, s43
	s_mul_i32 s32, s32, 3
	s_waitcnt lgkmcnt(0)
	s_add_u32 s56, s56, 0x4000000
	s_addc_u32 s57, s57, 0
	s_add_u32 s82, s82, 0x4000000
	s_addc_u32 s83, s83, 0
	s_add_u32 s38, s38, 0x4000000
	s_addc_u32 s39, s39, 0
	s_add_u32 s44, s44, 0x400000
	s_addc_u32 s45, s45, 0
	s_add_u32 s46, s46, 0x100000
	s_addc_u32 s47, s47, 0
	s_add_u32 s48, s48, 0x2bd00000
	s_addc_u32 s49, s49, 0
	s_mov_b32 s41, 0
	s_add_u32 s43, s32, 0
	s_cmp_lt_u32 s43, 0x6780
	s_cbranch_scc0 .Lcvb4_wait
	s_add_u32 s43, s32, 0
	s_cmp_lt_u32 s43, 0x300
	s_cbranch_scc0 .Lcvb4_d0_b
	s_mul_i32 s58, s43, 0xaaab
	s_lshr_b32 s58, s58, 21
	s_mul_i32 s59, s58, 48
	s_sub_u32 s59, s43, s59
	s_mul_i32 s60, s58, 0x60000
	s_mul_i32 s81, s59, 0x80
	s_add_u32 s60, s60, s81
	s_add_u32 s92, s94, s60
	s_addc_u32 s93, s95, 0
	s_mov_b32 s63, 0x1800
	s_mul_i32 s61, s59, 0x8000
	s_mul_i32 s81, s58, 0x40
	s_add_u32 s61, s61, s81
	s_add_u32 s61, s61, 0x800000
	s_add_u32 s50, s48, s61
	s_addc_u32 s51, s49, 0
	s_mov_b32 s65, 0x400
	s_mov_b32 s71, 0x44000000
	s_branch .Lcvb4_d0_ld

.LBB0_794:
	s_or_b64 exec, exec, s[0:1]
	v_readlane_b32 s12, v254, 1
	v_readlane_b32 s13, v254, 2
	v_readlane_b32 s69, v254, 41
	s_nop 3
	s_cmp_eq_u32 s69, 0
	s_cbranch_scc1 .Lcvb5_skip
	s_waitcnt vmcnt(0) lgkmcnt(0)
	v_readlane_b32 s0, v254, 42
	v_readlane_b32 s1, v254, 43
	v_readlane_b32 s60, v254, 0
	v_readlane_b32 s61, v254, 41
	s_nop 3
	s_sub_u32 s0, s0, 0xd0
	s_subb_u32 s1, s1, 0
	s_load_dwordx2 s[94:95], s[0:1], 0x20
	s_load_dwordx2 s[98:99], s[0:1], 0x28
	s_load_dwordx2 s[56:57], s[0:1], 0x88
	s_load_dwordx2 s[82:83], s[0:1], 0x90
	s_load_dwordx2 s[38:39], s[0:1], 0x98
	s_load_dwordx2 s[44:45], s[0:1], 0xa0
	s_load_dwordx2 s[46:47], s[0:1], 0xa8
	s_load_dwordx2 s[48:49], s[0:1], 0xb8
	v_mbcnt_lo_u32_b32 v100, -1, 0
	v_mbcnt_hi_u32_b32 v100, -1, v100
	v_and_b32_e32 v96, 7, v100
	v_lshrrev_b32_e32 v97, 3, v100
	v_mov_b32_e32 v98, 0x43e00000
	s_mov_b32 s64, 0xc3e00000
	s_mul_i32 s32, s60, 7
	s_add_u32 s32, s32, s61
	s_sub_u32 s32, s32, 1
	s_mul_i32 s43, s74, 28
	s_add_u32 s32, s32, s43
	s_mul_i32 s32, s32, 3
	s_waitcnt lgkmcnt(0)
	s_add_u32 s56, s56, 0x4000000
	s_addc_u32 s57, s57, 0
	s_add_u32 s82, s82, 0x4000000
	s_addc_u32 s83, s83, 0
	s_add_u32 s38, s38, 0x4000000
	s_addc_u32 s39, s39, 0
	s_add_u32 s44, s44, 0x400000
	s_addc_u32 s45, s45, 0
	s_add_u32 s46, s46, 0x100000
	s_addc_u32 s47, s47, 0
	s_add_u32 s48, s48, 0x2bd00000
	s_addc_u32 s49, s49, 0
	s_mov_b32 s41, 0
	s_add_u32 s43, s32, 0
	s_cmp_lt_u32 s43, 0x6780
	s_cbranch_scc0 .Lcvb5_wait
	s_add_u32 s43, s32, 0
	s_cmp_lt_u32 s43, 0x300
	s_cbranch_scc0 .Lcvb5_d0_b
	s_mul_i32 s58, s43, 0xaaab
	s_lshr_b32 s58, s58, 21
	s_mul_i32 s59, s58, 48
	s_sub_u32 s59, s43, s59
	s_mul_i32 s60, s58, 0x60000
	s_mul_i32 s81, s59, 0x80
	s_add_u32 s60, s60, s81
	s_add_u32 s92, s94, s60
	s_addc_u32 s93, s95, 0
	s_mov_b32 s63, 0x1800
	s_mul_i32 s61, s59, 0x8000
	s_mul_i32 s81, s58, 0x40
	s_add_u32 s61, s61, s81
	s_add_u32 s61, s61, 0x800000
	s_add_u32 s50, s48, s61
	s_addc_u32 s51, s49, 0
	s_mov_b32 s65, 0x400
	s_mov_b32 s71, 0x44000000
	s_branch .Lcvb5_d0_ld

.LBB0_892:
	s_or_b64 exec, exec, s[0:1]
	v_readlane_b32 s12, v254, 1
	v_readlane_b32 s13, v254, 2
	v_readlane_b32 s69, v254, 41
	s_nop 3
	s_cmp_eq_u32 s69, 0
	s_cbranch_scc1 .Lcvb6_skip
	s_waitcnt vmcnt(0) lgkmcnt(0)
	v_readlane_b32 s0, v254, 42
	v_readlane_b32 s1, v254, 43
	v_readlane_b32 s60, v254, 0
	v_readlane_b32 s61, v254, 41
	s_nop 3
	s_sub_u32 s0, s0, 0xd0
	s_subb_u32 s1, s1, 0
	s_load_dwordx2 s[94:95], s[0:1], 0x20
	s_load_dwordx2 s[98:99], s[0:1], 0x28
	s_load_dwordx2 s[56:57], s[0:1], 0x88
	s_load_dwordx2 s[82:83], s[0:1], 0x90
	s_load_dwordx2 s[38:39], s[0:1], 0x98
	s_load_dwordx2 s[44:45], s[0:1], 0xa0
	s_load_dwordx2 s[46:47], s[0:1], 0xa8
	s_load_dwordx2 s[48:49], s[0:1], 0xb8
	v_mbcnt_lo_u32_b32 v100, -1, 0
	v_mbcnt_hi_u32_b32 v100, -1, v100
	v_and_b32_e32 v96, 7, v100
	v_lshrrev_b32_e32 v97, 3, v100
	v_mov_b32_e32 v98, 0x43e00000
	s_mov_b32 s64, 0xc3e00000
	s_mul_i32 s32, s60, 7
	s_add_u32 s32, s32, s61
	s_sub_u32 s32, s32, 1
	s_mul_i32 s43, s74, 35
	s_add_u32 s32, s32, s43
	s_mul_i32 s32, s32, 3
	s_waitcnt lgkmcnt(0)
	s_add_u32 s56, s56, 0x4000000
	s_addc_u32 s57, s57, 0
	s_add_u32 s82, s82, 0x4000000
	s_addc_u32 s83, s83, 0
	s_add_u32 s38, s38, 0x4000000
	s_addc_u32 s39, s39, 0
	s_add_u32 s44, s44, 0x400000
	s_addc_u32 s45, s45, 0
	s_add_u32 s46, s46, 0x100000
	s_addc_u32 s47, s47, 0
	s_add_u32 s48, s48, 0x2bd00000
	s_addc_u32 s49, s49, 0
	s_mov_b32 s41, 0
	s_add_u32 s43, s32, 0
	s_cmp_lt_u32 s43, 0x6780
	s_cbranch_scc0 .Lcvb6_wait
	s_add_u32 s43, s32, 0
	s_cmp_lt_u32 s43, 0x300
	s_cbranch_scc0 .Lcvb6_d0_b
	s_mul_i32 s58, s43, 0xaaab
	s_lshr_b32 s58, s58, 21
	s_mul_i32 s59, s58, 48
	s_sub_u32 s59, s43, s59
	s_mul_i32 s60, s58, 0x60000
	s_mul_i32 s81, s59, 0x80
	s_add_u32 s60, s60, s81
	s_add_u32 s92, s94, s60
	s_addc_u32 s93, s95, 0
	s_mov_b32 s63, 0x1800
	s_mul_i32 s61, s59, 0x8000
	s_mul_i32 s81, s58, 0x40
	s_add_u32 s61, s61, s81
	s_add_u32 s61, s61, 0x800000
	s_add_u32 s50, s48, s61
	s_addc_u32 s51, s49, 0
	s_mov_b32 s65, 0x400
	s_mov_b32 s71, 0x44000000
	s_branch .Lcvb6_d0_ld

.LBB0_1235:
	s_or_b64 exec, exec, s[0:1]
	v_readlane_b32 s12, v254, 1
	v_readlane_b32 s13, v254, 2
	v_readlane_b32 s69, v254, 41
	s_nop 3
	s_cmp_eq_u32 s69, 0
	s_cbranch_scc1 .Lcvb11_skip
	s_waitcnt vmcnt(0) lgkmcnt(0)
	v_readlane_b32 s0, v254, 42
	v_readlane_b32 s1, v254, 43
	v_readlane_b32 s60, v254, 0
	v_readlane_b32 s61, v254, 41
	s_nop 3
	s_sub_u32 s0, s0, 0xd0
	s_subb_u32 s1, s1, 0
	s_load_dwordx2 s[94:95], s[0:1], 0x38
	s_load_dwordx2 s[98:99], s[0:1], 0x40
	s_load_dwordx2 s[56:57], s[0:1], 0x88
	s_load_dwordx2 s[82:83], s[0:1], 0x90
	s_load_dwordx2 s[38:39], s[0:1], 0x98
	s_load_dwordx2 s[44:45], s[0:1], 0xa0
	s_load_dwordx2 s[46:47], s[0:1], 0xa8
	s_load_dwordx2 s[48:49], s[0:1], 0xb8
	v_mbcnt_lo_u32_b32 v100, -1, 0
	v_mbcnt_hi_u32_b32 v100, -1, v100
	v_and_b32_e32 v96, 7, v100
	v_lshrrev_b32_e32 v97, 3, v100
	v_mov_b32_e32 v98, 0x43e00000
	s_mov_b32 s64, 0xc3e00000
	s_mul_i32 s32, s60, 7
	s_add_u32 s32, s32, s61
	s_sub_u32 s32, s32, 1
	s_mul_i32 s32, s32, 3
	s_waitcnt lgkmcnt(0)
	s_add_u32 s56, s56, 0x8000000
	s_addc_u32 s57, s57, 0
	s_add_u32 s82, s82, 0x8000000
	s_addc_u32 s83, s83, 0
	s_add_u32 s38, s38, 0x8000000
	s_addc_u32 s39, s39, 0
	s_add_u32 s44, s44, 0x800000
	s_addc_u32 s45, s45, 0
	s_add_u32 s46, s46, 0x200000
	s_addc_u32 s47, s47, 0
	s_mov_b32 s41, 0
	s_add_u32 s43, s32, 0
	s_cmp_lt_u32 s43, 0x6a80
	s_cbranch_scc0 .Lcvb11_wait
	s_add_u32 s43, s32, 0
	s_cmp_lt_u32 s43, 0x600
	s_cbranch_scc0 .Lcvb11_d0_b
	s_mul_i32 s58, s43, 0xaaab
	s_lshr_b32 s58, s58, 22
	s_mul_i32 s59, s58, 96
	s_sub_u32 s59, s43, s59
	s_mul_i32 s60, s58, 0xc0000
	s_mul_i32 s81, s59, 0x80
	s_add_u32 s60, s60, s81
	s_add_u32 s92, s94, s60
	s_addc_u32 s93, s95, 0
	s_mov_b32 s63, 0x3000
	s_mul_i32 s61, s59, 0x8000
	s_mul_i32 s81, s58, 0x40
	s_add_u32 s61, s61, s81
	s_add_u32 s61, s61, 0x800000
	s_add_u32 s50, s48, s61
	s_addc_u32 s51, s49, 0
	s_mov_b32 s65, 0x400
	s_mov_b32 s71, 0x44000000
	s_branch .Lcvb11_d0_ld
.Lcvb11_d0_b:
	s_sub_u32 s43, s43, 0x600
	s_cmp_lt_u32 s43, 0x200
	s_cbranch_scc0 .Lcvb11_d0_c
	s_lshr_b32 s58, s43, 5
	s_and_b32 s59, s43, 31
	s_mul_i32 s60, s58, 0x40000
	s_mul_i32 s81, s59, 0x80
	s_add_u32 s60, s60, s81
	s_add_u32 s92, s98, s60
	s_addc_u32 s93, s99, 0
	s_mov_b32 s63, 0x1000
	s_mul_i32 s61, s59, 0x8000
	s_mul_i32 s81, s58, 0x40
	s_add_u32 s61, s61, s81
	s_add_u32 s61, s61, 0xe00000
	s_add_u32 s50, s48, s61
	s_addc_u32 s51, s49, 0
	s_mov_b32 s65, 0x400
	s_mov_b32 s71, 0x44800000
	s_branch .Lcvb11_d0_ld

.Lcvb11_d0_ld:
	s_lshl_b32 s60, s63, 3
	v_mul_lo_u32 v0, v96, s60
	v_lshl_add_u32 v0, v97, 4, v0
	v_add_u32_e32 v4, s63, v0
	v_add_u32_e32 v10, s63, v4
	v_add_u32_e32 v11, s63, v10
	v_add_u32_e32 v12, s63, v11
	v_add_u32_e32 v19, s63, v12
	v_add_u32_e32 v24, s63, v19
	v_add_u32_e32 v25, s63, v24
	global_load_dwordx4 v[34:37], v0, s[92:93] nt
	global_load_dwordx4 v[38:41], v4, s[92:93] nt
	global_load_dwordx4 v[42:45], v10, s[92:93] nt
	global_load_dwordx4 v[46:49], v11, s[92:93] nt
	global_load_dwordx4 v[50:53], v12, s[92:93] nt
	global_load_dwordx4 v[54:57], v19, s[92:93] nt
	global_load_dwordx4 v[58:61], v24, s[92:93] nt
	global_load_dwordx4 v[62:65], v25, s[92:93] nt
	s_mov_b32 s41, 1
	s_add_u32 s43, s32, 1
	s_cmp_lt_u32 s43, 0x6a80
	s_cbranch_scc0 .Lcvb11_wait
	s_add_u32 s43, s32, 1
	s_cmp_lt_u32 s43, 0x600
	s_cbranch_scc0 .Lcvb11_d1_b
	s_mul_i32 s58, s43, 0xaaab
	s_lshr_b32 s58, s58, 22
	s_mul_i32 s59, s58, 96
	s_sub_u32 s59, s43, s59
	s_mul_i32 s60, s58, 0xc0000
	s_mul_i32 s81, s59, 0x80
	s_add_u32 s60, s60, s81
	s_add_u32 s92, s94, s60
	s_addc_u32 s93, s95, 0
	s_mov_b32 s63, 0x3000
	s_mul_i32 s61, s59, 0x8000
	s_mul_i32 s81, s58, 0x40
	s_add_u32 s61, s61, s81
	s_add_u32 s61, s61, 0x800000
	s_add_u32 s52, s48, s61
	s_addc_u32 s53, s49, 0
	s_mov_b32 s66, 0x400
	s_mov_b32 s75, 0x44000000
	s_branch .Lcvb11_d1_ld
.Lcvb11_d1_b:
	s_sub_u32 s43, s43, 0x600
	s_cmp_lt_u32 s43, 0x200
	s_cbranch_scc0 .Lcvb11_d1_c
	s_lshr_b32 s58, s43, 5
	s_and_b32 s59, s43, 31
	s_mul_i32 s60, s58, 0x40000
	s_mul_i32 s81, s59, 0x80
	s_add_u32 s60, s60, s81
	s_add_u32 s92, s98, s60
	s_addc_u32 s93, s99, 0
	s_mov_b32 s63, 0x1000
	s_mul_i32 s61, s59, 0x8000
	s_mul_i32 s81, s58, 0x40
	s_add_u32 s61, s61, s81
	s_add_u32 s61, s61, 0xe00000
	s_add_u32 s52, s48, s61
	s_addc_u32 s53, s49, 0
	s_mov_b32 s66, 0x400
	s_mov_b32 s75, 0x44800000
	s_branch .Lcvb11_d1_ld

.Lcvb11_d1_ld:
	s_lshl_b32 s60, s63, 3
	v_mul_lo_u32 v0, v96, s60
	v_lshl_add_u32 v0, v97, 4, v0
	v_add_u32_e32 v4, s63, v0
	v_add_u32_e32 v10, s63, v4
	v_add_u32_e32 v11, s63, v10
	v_add_u32_e32 v12, s63, v11
	v_add_u32_e32 v19, s63, v12
	v_add_u32_e32 v24, s63, v19
	v_add_u32_e32 v25, s63, v24
	global_load_dwordx4 v[66:69], v0, s[92:93] nt
	global_load_dwordx4 v[70:73], v4, s[92:93] nt
	global_load_dwordx4 v[74:77], v10, s[92:93] nt
	global_load_dwordx4 v[78:81], v11, s[92:93] nt
	global_load_dwordx4 v[82:85], v12, s[92:93] nt
	global_load_dwordx4 v[86:89], v19, s[92:93] nt
	global_load_dwordx4 v[102:105], v24, s[92:93] nt
	global_load_dwordx4 v[106:109], v25, s[92:93] nt
	s_mov_b32 s41, 2
	s_add_u32 s43, s32, 2
	s_cmp_lt_u32 s43, 0x6a80
	s_cbranch_scc0 .Lcvb11_wait
	s_add_u32 s43, s32, 2
	s_cmp_lt_u32 s43, 0x600
	s_cbranch_scc0 .Lcvb11_d2_b
	s_mul_i32 s58, s43, 0xaaab
	s_lshr_b32 s58, s58, 22
	s_mul_i32 s59, s58, 96
	s_sub_u32 s59, s43, s59
	s_mul_i32 s60, s58, 0xc0000
	s_mul_i32 s81, s59, 0x80
	s_add_u32 s60, s60, s81
	s_add_u32 s92, s94, s60
	s_addc_u32 s93, s95, 0
	s_mov_b32 s63, 0x3000
	s_mul_i32 s61, s59, 0x8000
	s_mul_i32 s81, s58, 0x40
	s_add_u32 s61, s61, s81
	s_add_u32 s61, s61, 0x800000
	s_add_u32 s54, s48, s61
	s_addc_u32 s55, s49, 0
	s_mov_b32 s67, 0x400
	s_mov_b32 s78, 0x44000000
	s_branch .Lcvb11_d2_ld
.Lcvb11_d2_b:
	s_sub_u32 s43, s43, 0x600
	s_cmp_lt_u32 s43, 0x200
	s_cbranch_scc0 .Lcvb11_d2_c
	s_lshr_b32 s58, s43, 5
	s_and_b32 s59, s43, 31
	s_mul_i32 s60, s58, 0x40000
	s_mul_i32 s81, s59, 0x80
	s_add_u32 s60, s60, s81
	s_add_u32 s92, s98, s60
	s_addc_u32 s93, s99, 0
	s_mov_b32 s63, 0x1000
	s_mul_i32 s61, s59, 0x8000
	s_mul_i32 s81, s58, 0x40
	s_add_u32 s61, s61, s81
	s_add_u32 s61, s61, 0xe00000
	s_add_u32 s54, s48, s61
	s_addc_u32 s55, s49, 0
	s_mov_b32 s67, 0x400
	s_mov_b32 s78, 0x44800000
	s_branch .Lcvb11_d2_ld

.Lcvt_site_1333:
	s_waitcnt vmcnt(0) lgkmcnt(0)
	v_readlane_b32 s0, v254, 42
	v_readlane_b32 s1, v254, 43
	v_readlane_b32 s60, v254, 0
	v_readlane_b32 s61, v254, 41
	s_nop 3
	s_sub_u32 s0, s0, 0xd0
	s_subb_u32 s1, s1, 0
	s_load_dwordx2 s[10:11], s[0:1], 0x38
	s_load_dwordx2 s[12:13], s[0:1], 0x40
	s_load_dwordx2 s[14:15], s[0:1], 0x88
	s_load_dwordx2 s[28:29], s[0:1], 0x90
	s_load_dwordx2 s[38:39], s[0:1], 0x98
	s_load_dwordx2 s[44:45], s[0:1], 0xa0
	s_load_dwordx2 s[46:47], s[0:1], 0xa8
	s_load_dwordx2 s[48:49], s[0:1], 0xb8
	v_mbcnt_lo_u32_b32 v100, -1, 0
	v_mbcnt_hi_u32_b32 v100, -1, v100
	v_and_b32_e32 v96, 7, v100
	v_lshrrev_b32_e32 v97, 3, v100
	v_mov_b32_e32 v98, 0x43e00000
	s_mov_b32 s64, 0xc3e00000
	s_lshl_b32 s9, s60, 3
	s_add_u32 s9, s9, s61
	s_min_u32 s20, s74, 0x80
	s_lshl_b32 s20, s20, 5
	s_waitcnt lgkmcnt(0)
	s_add_u32 s14, s14, 0x8000000
	s_addc_u32 s15, s15, 0
	s_add_u32 s28, s28, 0x8000000
	s_addc_u32 s29, s29, 0
	s_add_u32 s38, s38, 0x8000000
	s_addc_u32 s39, s39, 0
	s_add_u32 s44, s44, 0x800000
	s_addc_u32 s45, s45, 0
	s_add_u32 s46, s46, 0x200000
	s_addc_u32 s47, s47, 0
	s_mul_i32 s32, s74, 126
	s_lshl_b32 s60, s9, 2
	s_add_u32 s32, s32, s60
	s_mov_b32 s41, 0
	s_cmp_lt_u32 s32, 0x6a80
	s_cbranch_scc0 .Lcv1333_drain0
	s_add_u32 s43, s32, 0
	s_cmp_lt_u32 s43, 0x600
	s_cbranch_scc0 .Lcv1333_d0_b
	s_mul_i32 s58, s43, 0xaaab
	s_lshr_b32 s58, s58, 22
	s_mul_i32 s59, s58, 96
	s_sub_u32 s59, s43, s59
	s_mul_i32 s60, s58, 0xc0000
	s_mul_i32 s81, s59, 0x80
	s_add_u32 s60, s60, s81
	s_add_u32 s2, s10, s60
	s_addc_u32 s3, s11, 0
	s_mov_b32 s63, 0x3000
	s_mul_i32 s61, s59, 0x8000
	s_mul_i32 s81, s58, 0x40
	s_add_u32 s61, s61, s81
	s_add_u32 s61, s61, 0x800000
	s_add_u32 s50, s48, s61
	s_addc_u32 s51, s49, 0
	s_mov_b32 s65, 0x400
	s_mov_b32 s71, 0x44000000
	s_branch .Lcv1333_d0_ld

.LBB0_1482:
	s_or_b64 exec, exec, s[0:1]
	v_readlane_b32 s12, v254, 1
	v_readlane_b32 s13, v254, 2
	v_readlane_b32 s69, v254, 41
	s_nop 3
	s_cmp_eq_u32 s69, 0
	s_cbranch_scc1 .Lcvb13_skip
	s_waitcnt vmcnt(0) lgkmcnt(0)
	v_readlane_b32 s0, v254, 42
	v_readlane_b32 s1, v254, 43
	v_readlane_b32 s60, v254, 0
	v_readlane_b32 s61, v254, 41
	s_nop 3
	s_sub_u32 s0, s0, 0xd0
	s_subb_u32 s1, s1, 0
	s_load_dwordx2 s[94:95], s[0:1], 0x38
	s_load_dwordx2 s[98:99], s[0:1], 0x40
	s_load_dwordx2 s[56:57], s[0:1], 0x88
	s_load_dwordx2 s[82:83], s[0:1], 0x90
	s_load_dwordx2 s[38:39], s[0:1], 0x98
	s_load_dwordx2 s[44:45], s[0:1], 0xa0
	s_load_dwordx2 s[46:47], s[0:1], 0xa8
	s_load_dwordx2 s[48:49], s[0:1], 0xb8
	v_mbcnt_lo_u32_b32 v100, -1, 0
	v_mbcnt_hi_u32_b32 v100, -1, v100
	v_and_b32_e32 v96, 7, v100
	v_lshrrev_b32_e32 v97, 3, v100
	v_mov_b32_e32 v98, 0x43e00000
	s_mov_b32 s64, 0xc3e00000
	s_mul_i32 s32, s60, 7
	s_add_u32 s32, s32, s61
	s_sub_u32 s32, s32, 1
	s_mul_i32 s43, s74, 7
	s_add_u32 s32, s32, s43
	s_mul_i32 s32, s32, 3
	s_waitcnt lgkmcnt(0)
	s_add_u32 s56, s56, 0x8000000
	s_addc_u32 s57, s57, 0
	s_add_u32 s82, s82, 0x8000000
	s_addc_u32 s83, s83, 0
	s_add_u32 s38, s38, 0x8000000
	s_addc_u32 s39, s39, 0
	s_add_u32 s44, s44, 0x800000
	s_addc_u32 s45, s45, 0
	s_add_u32 s46, s46, 0x200000
	s_addc_u32 s47, s47, 0
	s_mov_b32 s41, 0
	s_add_u32 s43, s32, 0
	s_cmp_lt_u32 s43, 0x6a80
	s_cbranch_scc0 .Lcvb13_wait
	s_add_u32 s43, s32, 0
	s_cmp_lt_u32 s43, 0x600
	s_cbranch_scc0 .Lcvb13_d0_b
	s_mul_i32 s58, s43, 0xaaab
	s_lshr_b32 s58, s58, 22
	s_mul_i32 s59, s58, 96
	s_sub_u32 s59, s43, s59
	s_mul_i32 s60, s58, 0xc0000
	s_mul_i32 s81, s59, 0x80
	s_add_u32 s60, s60, s81
	s_add_u32 s92, s94, s60
	s_addc_u32 s93, s95, 0
	s_mov_b32 s63, 0x3000
	s_mul_i32 s61, s59, 0x8000
	s_mul_i32 s81, s58, 0x40
	s_add_u32 s61, s61, s81
	s_add_u32 s61, s61, 0x800000
	s_add_u32 s50, s48, s61
	s_addc_u32 s51, s49, 0
	s_mov_b32 s65, 0x400
	s_mov_b32 s71, 0x44000000
	s_branch .Lcvb13_d0_ld

.LBB0_1601:
	s_or_b64 exec, exec, s[0:1]
	v_readlane_b32 s12, v254, 1
	v_readlane_b32 s13, v254, 2
	v_readlane_b32 s69, v254, 41
	s_nop 3
	s_cmp_eq_u32 s69, 0
	s_cbranch_scc1 .Lcvb14_skip
	s_waitcnt vmcnt(0) lgkmcnt(0)
	v_readlane_b32 s0, v254, 42
	v_readlane_b32 s1, v254, 43
	v_readlane_b32 s60, v254, 0
	v_readlane_b32 s61, v254, 41
	s_nop 3
	s_sub_u32 s0, s0, 0xd0
	s_subb_u32 s1, s1, 0
	s_load_dwordx2 s[94:95], s[0:1], 0x38
	s_load_dwordx2 s[98:99], s[0:1], 0x40
	s_load_dwordx2 s[56:57], s[0:1], 0x88
	s_load_dwordx2 s[82:83], s[0:1], 0x90
	s_load_dwordx2 s[38:39], s[0:1], 0x98
	s_load_dwordx2 s[44:45], s[0:1], 0xa0
	s_load_dwordx2 s[46:47], s[0:1], 0xa8
	s_load_dwordx2 s[48:49], s[0:1], 0xb8
	v_mbcnt_lo_u32_b32 v100, -1, 0
	v_mbcnt_hi_u32_b32 v100, -1, v100
	v_and_b32_e32 v96, 7, v100
	v_lshrrev_b32_e32 v97, 3, v100
	v_mov_b32_e32 v98, 0x43e00000
	s_mov_b32 s64, 0xc3e00000
	s_mul_i32 s32, s60, 7
	s_add_u32 s32, s32, s61
	s_sub_u32 s32, s32, 1
	s_mul_i32 s43, s74, 14
	s_add_u32 s32, s32, s43
	s_mul_i32 s32, s32, 3
	s_waitcnt lgkmcnt(0)
	s_add_u32 s56, s56, 0x8000000
	s_addc_u32 s57, s57, 0
	s_add_u32 s82, s82, 0x8000000
	s_addc_u32 s83, s83, 0
	s_add_u32 s38, s38, 0x8000000
	s_addc_u32 s39, s39, 0
	s_add_u32 s44, s44, 0x800000
	s_addc_u32 s45, s45, 0
	s_add_u32 s46, s46, 0x200000
	s_addc_u32 s47, s47, 0
	s_mov_b32 s41, 0
	s_add_u32 s43, s32, 0
	s_cmp_lt_u32 s43, 0x6a80
	s_cbranch_scc0 .Lcvb14_wait
	s_add_u32 s43, s32, 0
	s_cmp_lt_u32 s43, 0x600
	s_cbranch_scc0 .Lcvb14_d0_b
	s_mul_i32 s58, s43, 0xaaab
	s_lshr_b32 s58, s58, 22
	s_mul_i32 s59, s58, 96
	s_sub_u32 s59, s43, s59
	s_mul_i32 s60, s58, 0xc0000
	s_mul_i32 s81, s59, 0x80
	s_add_u32 s60, s60, s81
	s_add_u32 s92, s94, s60
	s_addc_u32 s93, s95, 0
	s_mov_b32 s63, 0x3000
	s_mul_i32 s61, s59, 0x8000
	s_mul_i32 s81, s58, 0x40
	s_add_u32 s61, s61, s81
	s_add_u32 s61, s61, 0x800000
	s_add_u32 s50, s48, s61
	s_addc_u32 s51, s49, 0
	s_mov_b32 s65, 0x400
	s_mov_b32 s71, 0x44000000
	s_branch .Lcvb14_d0_ld

.LBB0_1671:
	s_or_b64 exec, exec, s[0:1]
	v_readlane_b32 s12, v254, 1
	v_readlane_b32 s13, v254, 2
	v_readlane_b32 s69, v254, 41
	s_nop 3
	s_cmp_eq_u32 s69, 0
	s_cbranch_scc1 .Lcvb15_skip
	s_waitcnt vmcnt(0) lgkmcnt(0)
	v_readlane_b32 s0, v254, 42
	v_readlane_b32 s1, v254, 43
	v_readlane_b32 s60, v254, 0
	v_readlane_b32 s61, v254, 41
	s_nop 3
	s_sub_u32 s0, s0, 0xd0
	s_subb_u32 s1, s1, 0
	s_load_dwordx2 s[94:95], s[0:1], 0x38
	s_load_dwordx2 s[98:99], s[0:1], 0x40
	s_load_dwordx2 s[56:57], s[0:1], 0x88
	s_load_dwordx2 s[82:83], s[0:1], 0x90
	s_load_dwordx2 s[38:39], s[0:1], 0x98
	s_load_dwordx2 s[44:45], s[0:1], 0xa0
	s_load_dwordx2 s[46:47], s[0:1], 0xa8
	s_load_dwordx2 s[48:49], s[0:1], 0xb8
	v_mbcnt_lo_u32_b32 v100, -1, 0
	v_mbcnt_hi_u32_b32 v100, -1, v100
	v_and_b32_e32 v96, 7, v100
	v_lshrrev_b32_e32 v97, 3, v100
	v_mov_b32_e32 v98, 0x43e00000
	s_mov_b32 s64, 0xc3e00000
	s_mul_i32 s32, s60, 7
	s_add_u32 s32, s32, s61
	s_sub_u32 s32, s32, 1
	s_mul_i32 s43, s74, 21
	s_add_u32 s32, s32, s43
	s_mul_i32 s32, s32, 3
	s_waitcnt lgkmcnt(0)
	s_add_u32 s56, s56, 0x8000000
	s_addc_u32 s57, s57, 0
	s_add_u32 s82, s82, 0x8000000
	s_addc_u32 s83, s83, 0
	s_add_u32 s38, s38, 0x8000000
	s_addc_u32 s39, s39, 0
	s_add_u32 s44, s44, 0x800000
	s_addc_u32 s45, s45, 0
	s_add_u32 s46, s46, 0x200000
	s_addc_u32 s47, s47, 0
	s_mov_b32 s41, 0
	s_add_u32 s43, s32, 0
	s_cmp_lt_u32 s43, 0x6a80
	s_cbranch_scc0 .Lcvb15_wait
	s_add_u32 s43, s32, 0
	s_cmp_lt_u32 s43, 0x600
	s_cbranch_scc0 .Lcvb15_d0_b
	s_mul_i32 s58, s43, 0xaaab
	s_lshr_b32 s58, s58, 22
	s_mul_i32 s59, s58, 96
	s_sub_u32 s59, s43, s59
	s_mul_i32 s60, s58, 0xc0000
	s_mul_i32 s81, s59, 0x80
	s_add_u32 s60, s60, s81
	s_add_u32 s92, s94, s60
	s_addc_u32 s93, s95, 0
	s_mov_b32 s63, 0x3000
	s_mul_i32 s61, s59, 0x8000
	s_mul_i32 s81, s58, 0x40
	s_add_u32 s61, s61, s81
	s_add_u32 s61, s61, 0x800000
	s_add_u32 s50, s48, s61
	s_addc_u32 s51, s49, 0
	s_mov_b32 s65, 0x400
	s_mov_b32 s71, 0x44000000
	s_branch .Lcvb15_d0_ld

.LBB0_1769:
	s_or_b64 exec, exec, s[0:1]
	v_readlane_b32 s12, v254, 1
	v_readlane_b32 s13, v254, 2
	v_readlane_b32 s69, v254, 41
	s_nop 3
	s_cmp_eq_u32 s69, 0
	s_cbranch_scc1 .Lcvb16_skip
	s_waitcnt vmcnt(0) lgkmcnt(0)
	v_readlane_b32 s0, v254, 42
	v_readlane_b32 s1, v254, 43
	v_readlane_b32 s60, v254, 0
	v_readlane_b32 s61, v254, 41
	s_nop 3
	s_sub_u32 s0, s0, 0xd0
	s_subb_u32 s1, s1, 0
	s_load_dwordx2 s[94:95], s[0:1], 0x38
	s_load_dwordx2 s[98:99], s[0:1], 0x40
	s_load_dwordx2 s[56:57], s[0:1], 0x88
	s_load_dwordx2 s[82:83], s[0:1], 0x90
	s_load_dwordx2 s[38:39], s[0:1], 0x98
	s_load_dwordx2 s[44:45], s[0:1], 0xa0
	s_load_dwordx2 s[46:47], s[0:1], 0xa8
	s_load_dwordx2 s[48:49], s[0:1], 0xb8
	v_mbcnt_lo_u32_b32 v100, -1, 0
	v_mbcnt_hi_u32_b32 v100, -1, v100
	v_and_b32_e32 v96, 7, v100
	v_lshrrev_b32_e32 v97, 3, v100
	v_mov_b32_e32 v98, 0x43e00000
	s_mov_b32 s64, 0xc3e00000
	s_mul_i32 s32, s60, 7
	s_add_u32 s32, s32, s61
	s_sub_u32 s32, s32, 1
	s_mul_i32 s43, s74, 28
	s_add_u32 s32, s32, s43
	s_mul_i32 s32, s32, 3
	s_waitcnt lgkmcnt(0)
	s_add_u32 s56, s56, 0x8000000
	s_addc_u32 s57, s57, 0
	s_add_u32 s82, s82, 0x8000000
	s_addc_u32 s83, s83, 0
	s_add_u32 s38, s38, 0x8000000
	s_addc_u32 s39, s39, 0
	s_add_u32 s44, s44, 0x800000
	s_addc_u32 s45, s45, 0
	s_add_u32 s46, s46, 0x200000
	s_addc_u32 s47, s47, 0
	s_mov_b32 s41, 0
	s_add_u32 s43, s32, 0
	s_cmp_lt_u32 s43, 0x6a80
	s_cbranch_scc0 .Lcvb16_wait
	s_add_u32 s43, s32, 0
	s_cmp_lt_u32 s43, 0x600
	s_cbranch_scc0 .Lcvb16_d0_b
	s_mul_i32 s58, s43, 0xaaab
	s_lshr_b32 s58, s58, 22
	s_mul_i32 s59, s58, 96
	s_sub_u32 s59, s43, s59
	s_mul_i32 s60, s58, 0xc0000
	s_mul_i32 s81, s59, 0x80
	s_add_u32 s60, s60, s81
	s_add_u32 s92, s94, s60
	s_addc_u32 s93, s95, 0
	s_mov_b32 s63, 0x3000
	s_mul_i32 s61, s59, 0x8000
	s_mul_i32 s81, s58, 0x40
	s_add_u32 s61, s61, s81
	s_add_u32 s61, s61, 0x800000
	s_add_u32 s50, s48, s61
	s_addc_u32 s51, s49, 0
	s_mov_b32 s65, 0x400
	s_mov_b32 s71, 0x44000000
	s_branch .Lcvb16_d0_ld

.LBB0_1859:
	s_or_b64 exec, exec, s[0:1]
	v_readlane_b32 s12, v254, 1
	v_readlane_b32 s13, v254, 2
	v_readlane_b32 s69, v254, 41
	s_nop 3
	s_cmp_eq_u32 s69, 0
	s_cbranch_scc1 .Lcvb17_skip
	s_waitcnt vmcnt(0) lgkmcnt(0)
	v_readlane_b32 s0, v254, 42
	v_readlane_b32 s1, v254, 43
	v_readlane_b32 s60, v254, 0
	v_readlane_b32 s61, v254, 41
	s_nop 3
	s_sub_u32 s0, s0, 0xd0
	s_subb_u32 s1, s1, 0
	s_load_dwordx2 s[94:95], s[0:1], 0x38
	s_load_dwordx2 s[98:99], s[0:1], 0x40
	s_load_dwordx2 s[56:57], s[0:1], 0x88
	s_load_dwordx2 s[82:83], s[0:1], 0x90
	s_load_dwordx2 s[38:39], s[0:1], 0x98
	s_load_dwordx2 s[44:45], s[0:1], 0xa0
	s_load_dwordx2 s[46:47], s[0:1], 0xa8
	s_load_dwordx2 s[48:49], s[0:1], 0xb8
	v_mbcnt_lo_u32_b32 v100, -1, 0
	v_mbcnt_hi_u32_b32 v100, -1, v100
	v_and_b32_e32 v96, 7, v100
	v_lshrrev_b32_e32 v97, 3, v100
	v_mov_b32_e32 v98, 0x43e00000
	s_mov_b32 s64, 0xc3e00000
	s_mul_i32 s32, s60, 7
	s_add_u32 s32, s32, s61
	s_sub_u32 s32, s32, 1
	s_mul_i32 s43, s74, 35
	s_add_u32 s32, s32, s43
	s_mul_i32 s32, s32, 3
	s_waitcnt lgkmcnt(0)
	s_add_u32 s56, s56, 0x8000000
	s_addc_u32 s57, s57, 0
	s_add_u32 s82, s82, 0x8000000
	s_addc_u32 s83, s83, 0
	s_add_u32 s38, s38, 0x8000000
	s_addc_u32 s39, s39, 0
	s_add_u32 s44, s44, 0x800000
	s_addc_u32 s45, s45, 0
	s_add_u32 s46, s46, 0x200000
	s_addc_u32 s47, s47, 0
	s_mov_b32 s41, 0
	s_add_u32 s43, s32, 0
	s_cmp_lt_u32 s43, 0x6a80
	s_cbranch_scc0 .Lcvb17_wait
	s_add_u32 s43, s32, 0
	s_cmp_lt_u32 s43, 0x600
	s_cbranch_scc0 .Lcvb17_d0_b
	s_mul_i32 s58, s43, 0xaaab
	s_lshr_b32 s58, s58, 22
	s_mul_i32 s59, s58, 96
	s_sub_u32 s59, s43, s59
	s_mul_i32 s60, s58, 0xc0000
	s_mul_i32 s81, s59, 0x80
	s_add_u32 s60, s60, s81
	s_add_u32 s92, s94, s60
	s_addc_u32 s93, s95, 0
	s_mov_b32 s63, 0x3000
	s_mul_i32 s61, s59, 0x8000
	s_mul_i32 s81, s58, 0x40
	s_add_u32 s61, s61, s81
	s_add_u32 s61, s61, 0x800000
	s_add_u32 s50, s48, s61
	s_addc_u32 s51, s49, 0
	s_mov_b32 s65, 0x400
	s_mov_b32 s71, 0x44000000
	s_branch .Lcvb17_d0_ld

.LBB0_2112:
	s_or_b64 exec, exec, s[0:1]
	v_readlane_b32 s12, v254, 1
	v_readlane_b32 s13, v254, 2
	v_readlane_b32 s69, v254, 41
	s_nop 3
	s_cmp_eq_u32 s69, 0
	s_cbranch_scc1 .Lcvb21_skip
	s_waitcnt vmcnt(0) lgkmcnt(0)
	v_readlane_b32 s0, v254, 42
	v_readlane_b32 s1, v254, 43
	v_readlane_b32 s60, v254, 0
	v_readlane_b32 s61, v254, 41
	s_nop 3
	s_sub_u32 s0, s0, 0xd0
	s_subb_u32 s1, s1, 0
	s_load_dwordx2 s[94:95], s[0:1], 0x10
	s_load_dwordx2 s[98:99], s[0:1], 0x18
	s_load_dwordx2 s[56:57], s[0:1], 0x88
	s_load_dwordx2 s[82:83], s[0:1], 0x90
	s_load_dwordx2 s[38:39], s[0:1], 0x98
	s_load_dwordx2 s[44:45], s[0:1], 0xa0
	s_load_dwordx2 s[46:47], s[0:1], 0xa8
	s_load_dwordx2 s[48:49], s[0:1], 0xb8
	v_mbcnt_lo_u32_b32 v100, -1, 0
	v_mbcnt_hi_u32_b32 v100, -1, v100
	v_and_b32_e32 v96, 7, v100
	v_lshrrev_b32_e32 v97, 3, v100
	v_mov_b32_e32 v98, 0x43e00000
	s_mov_b32 s64, 0xc3e00000
	s_mul_i32 s32, s60, 7
	s_add_u32 s32, s32, s61
	s_sub_u32 s32, s32, 1
	s_mul_i32 s32, s32, 3
	s_waitcnt lgkmcnt(0)
	s_add_u32 s94, s94, 0xc00000
	s_addc_u32 s95, s95, 0
	s_add_u32 s98, s98, 0x400000
	s_addc_u32 s99, s99, 0
	s_add_u32 s56, s56, 0xc000000
	s_addc_u32 s57, s57, 0
	s_add_u32 s82, s82, 0xc000000
	s_addc_u32 s83, s83, 0
	s_add_u32 s38, s38, 0xc000000
	s_addc_u32 s39, s39, 0
	s_add_u32 s44, s44, 0xc00000
	s_addc_u32 s45, s45, 0
	s_add_u32 s46, s46, 0x300000
	s_addc_u32 s47, s47, 0
	s_add_u32 s48, s48, 0x2bd00000
	s_addc_u32 s49, s49, 0
	s_mov_b32 s41, 0
	s_add_u32 s43, s32, 0
	s_cmp_lt_u32 s43, 0x6a80
	s_cbranch_scc0 .Lcvb21_wait
	s_add_u32 s43, s32, 0
	s_cmp_lt_u32 s43, 0x600
	s_cbranch_scc0 .Lcvb21_d0_b
	s_mul_i32 s58, s43, 0xaaab
	s_lshr_b32 s58, s58, 22
	s_mul_i32 s59, s58, 96
	s_sub_u32 s59, s43, s59
	s_mul_i32 s60, s58, 0xc0000
	s_mul_i32 s81, s59, 0x80
	s_add_u32 s60, s60, s81
	s_add_u32 s92, s94, s60
	s_addc_u32 s93, s95, 0
	s_mov_b32 s63, 0x3000
	s_mul_i32 s61, s59, 0x8000
	s_mul_i32 s81, s58, 0x40
	s_add_u32 s61, s61, s81
	s_add_u32 s61, s61, 0x800000
	s_add_u32 s50, s48, s61
	s_addc_u32 s51, s49, 0
	s_mov_b32 s65, 0x400
	s_mov_b32 s71, 0x44000000
	s_branch .Lcvb21_d0_ld

.Lcvt_site_2210:
	s_waitcnt vmcnt(0) lgkmcnt(0)
	v_readlane_b32 s0, v254, 42
	v_readlane_b32 s1, v254, 43
	v_readlane_b32 s60, v254, 0
	v_readlane_b32 s61, v254, 41
	s_nop 3
	s_sub_u32 s0, s0, 0xd0
	s_subb_u32 s1, s1, 0
	s_load_dwordx2 s[10:11], s[0:1], 0x10
	s_load_dwordx2 s[12:13], s[0:1], 0x18
	s_load_dwordx2 s[14:15], s[0:1], 0x88
	s_load_dwordx2 s[28:29], s[0:1], 0x90
	s_load_dwordx2 s[38:39], s[0:1], 0x98
	s_load_dwordx2 s[44:45], s[0:1], 0xa0
	s_load_dwordx2 s[46:47], s[0:1], 0xa8
	s_load_dwordx2 s[48:49], s[0:1], 0xb8
	v_mbcnt_lo_u32_b32 v100, -1, 0
	v_mbcnt_hi_u32_b32 v100, -1, v100
	v_and_b32_e32 v96, 7, v100
	v_lshrrev_b32_e32 v97, 3, v100
	v_mov_b32_e32 v98, 0x43e00000
	s_mov_b32 s64, 0xc3e00000
	s_lshl_b32 s9, s60, 3
	s_add_u32 s9, s9, s61
	s_min_u32 s20, s74, 0x40
	s_lshl_b32 s20, s20, 5
	s_waitcnt lgkmcnt(0)
	s_add_u32 s10, s10, 0xc00000
	s_addc_u32 s11, s11, 0
	s_add_u32 s12, s12, 0x400000
	s_addc_u32 s13, s13, 0
	s_add_u32 s14, s14, 0xc000000
	s_addc_u32 s15, s15, 0
	s_add_u32 s28, s28, 0xc000000
	s_addc_u32 s29, s29, 0
	s_add_u32 s38, s38, 0xc000000
	s_addc_u32 s39, s39, 0
	s_add_u32 s44, s44, 0xc00000
	s_addc_u32 s45, s45, 0
	s_add_u32 s46, s46, 0x300000
	s_addc_u32 s47, s47, 0
	s_add_u32 s48, s48, 0x2bd00000
	s_addc_u32 s49, s49, 0
	s_mul_i32 s32, s74, 126
	s_lshl_b32 s60, s9, 2
	s_add_u32 s32, s32, s60
	s_mov_b32 s41, 0
	s_cmp_lt_u32 s32, 0x6a80
	s_cbranch_scc0 .Lcv2210_drain0
	s_add_u32 s43, s32, 0
	s_cmp_lt_u32 s43, 0x600
	s_cbranch_scc0 .Lcv2210_d0_b
	s_mul_i32 s58, s43, 0xaaab
	s_lshr_b32 s58, s58, 22
	s_mul_i32 s59, s58, 96
	s_sub_u32 s59, s43, s59
	s_mul_i32 s60, s58, 0xc0000
	s_mul_i32 s81, s59, 0x80
	s_add_u32 s60, s60, s81
	s_add_u32 s2, s10, s60
	s_addc_u32 s3, s11, 0
	s_mov_b32 s63, 0x3000
	s_mul_i32 s61, s59, 0x8000
	s_mul_i32 s81, s58, 0x40
	s_add_u32 s61, s61, s81
	s_add_u32 s61, s61, 0x800000
	s_add_u32 s50, s48, s61
	s_addc_u32 s51, s49, 0
	s_mov_b32 s65, 0x400
	s_mov_b32 s71, 0x44000000
	s_branch .Lcv2210_d0_ld

.LBB0_2361:
	s_or_b64 exec, exec, s[0:1]
	v_readlane_b32 s12, v254, 1
	v_readlane_b32 s13, v254, 2
	v_readlane_b32 s69, v254, 41
	s_nop 3
	s_cmp_eq_u32 s69, 0
	s_cbranch_scc1 .Lcvb23_skip
	s_waitcnt vmcnt(0) lgkmcnt(0)
	v_readlane_b32 s0, v254, 42
	v_readlane_b32 s1, v254, 43
	v_readlane_b32 s60, v254, 0
	v_readlane_b32 s61, v254, 41
	s_nop 3
	s_sub_u32 s0, s0, 0xd0
	s_subb_u32 s1, s1, 0
	s_load_dwordx2 s[94:95], s[0:1], 0x10
	s_load_dwordx2 s[98:99], s[0:1], 0x18
	s_load_dwordx2 s[56:57], s[0:1], 0x88
	s_load_dwordx2 s[82:83], s[0:1], 0x90
	s_load_dwordx2 s[38:39], s[0:1], 0x98
	s_load_dwordx2 s[44:45], s[0:1], 0xa0
	s_load_dwordx2 s[46:47], s[0:1], 0xa8
	s_load_dwordx2 s[48:49], s[0:1], 0xb8
	v_mbcnt_lo_u32_b32 v100, -1, 0
	v_mbcnt_hi_u32_b32 v100, -1, v100
	v_and_b32_e32 v96, 7, v100
	v_lshrrev_b32_e32 v97, 3, v100
	v_mov_b32_e32 v98, 0x43e00000
	s_mov_b32 s64, 0xc3e00000
	s_mul_i32 s32, s60, 7
	s_add_u32 s32, s32, s61
	s_sub_u32 s32, s32, 1
	s_mul_i32 s43, s74, 7
	s_add_u32 s32, s32, s43
	s_mul_i32 s32, s32, 3
	s_waitcnt lgkmcnt(0)
	s_add_u32 s94, s94, 0xc00000
	s_addc_u32 s95, s95, 0
	s_add_u32 s98, s98, 0x400000
	s_addc_u32 s99, s99, 0
	s_add_u32 s56, s56, 0xc000000
	s_addc_u32 s57, s57, 0
	s_add_u32 s82, s82, 0xc000000
	s_addc_u32 s83, s83, 0
	s_add_u32 s38, s38, 0xc000000
	s_addc_u32 s39, s39, 0
	s_add_u32 s44, s44, 0xc00000
	s_addc_u32 s45, s45, 0
	s_add_u32 s46, s46, 0x300000
	s_addc_u32 s47, s47, 0
	s_add_u32 s48, s48, 0x2bd00000
	s_addc_u32 s49, s49, 0
	s_mov_b32 s41, 0
	s_add_u32 s43, s32, 0
	s_cmp_lt_u32 s43, 0x6a80
	s_cbranch_scc0 .Lcvb23_wait
	s_add_u32 s43, s32, 0
	s_cmp_lt_u32 s43, 0x600
	s_cbranch_scc0 .Lcvb23_d0_b
	s_mul_i32 s58, s43, 0xaaab
	s_lshr_b32 s58, s58, 22
	s_mul_i32 s59, s58, 96
	s_sub_u32 s59, s43, s59
	s_mul_i32 s60, s58, 0xc0000
	s_mul_i32 s81, s59, 0x80
	s_add_u32 s60, s60, s81
	s_add_u32 s92, s94, s60
	s_addc_u32 s93, s95, 0
	s_mov_b32 s63, 0x3000
	s_mul_i32 s61, s59, 0x8000
	s_mul_i32 s81, s58, 0x40
	s_add_u32 s61, s61, s81
	s_add_u32 s61, s61, 0x800000
	s_add_u32 s50, s48, s61
	s_addc_u32 s51, s49, 0
	s_mov_b32 s65, 0x400
	s_mov_b32 s71, 0x44000000
	s_branch .Lcvb23_d0_ld

.LBB0_2480:
	s_or_b64 exec, exec, s[0:1]
	v_readlane_b32 s69, v254, 41
	s_nop 3
	s_cmp_eq_u32 s69, 0
	s_cbranch_scc1 .Lcvb24_skip
	s_waitcnt vmcnt(0) lgkmcnt(0)
	v_readlane_b32 s0, v254, 42
	v_readlane_b32 s1, v254, 43
	v_readlane_b32 s60, v254, 0
	v_readlane_b32 s61, v254, 41
	s_nop 3
	s_sub_u32 s0, s0, 0xd0
	s_subb_u32 s1, s1, 0
	s_load_dwordx2 s[94:95], s[0:1], 0x10
	s_load_dwordx2 s[98:99], s[0:1], 0x18
	s_load_dwordx2 s[56:57], s[0:1], 0x88
	s_load_dwordx2 s[82:83], s[0:1], 0x90
	s_load_dwordx2 s[38:39], s[0:1], 0x98
	s_load_dwordx2 s[44:45], s[0:1], 0xa0
	s_load_dwordx2 s[46:47], s[0:1], 0xa8
	s_load_dwordx2 s[48:49], s[0:1], 0xb8
	v_mbcnt_lo_u32_b32 v100, -1, 0
	v_mbcnt_hi_u32_b32 v100, -1, v100
	v_and_b32_e32 v96, 7, v100
	v_lshrrev_b32_e32 v97, 3, v100
	v_mov_b32_e32 v98, 0x43e00000
	s_mov_b32 s64, 0xc3e00000
	s_mul_i32 s32, s60, 7
	s_add_u32 s32, s32, s61
	s_sub_u32 s32, s32, 1
	s_mul_i32 s43, s74, 14
	s_add_u32 s32, s32, s43
	s_mul_i32 s32, s32, 3
	s_waitcnt lgkmcnt(0)
	s_add_u32 s94, s94, 0xc00000
	s_addc_u32 s95, s95, 0
	s_add_u32 s98, s98, 0x400000
	s_addc_u32 s99, s99, 0
	s_add_u32 s56, s56, 0xc000000
	s_addc_u32 s57, s57, 0
	s_add_u32 s82, s82, 0xc000000
	s_addc_u32 s83, s83, 0
	s_add_u32 s38, s38, 0xc000000
	s_addc_u32 s39, s39, 0
	s_add_u32 s44, s44, 0xc00000
	s_addc_u32 s45, s45, 0
	s_add_u32 s46, s46, 0x300000
	s_addc_u32 s47, s47, 0
	s_add_u32 s48, s48, 0x2bd00000
	s_addc_u32 s49, s49, 0
	s_mov_b32 s41, 0
	s_add_u32 s43, s32, 0
	s_cmp_lt_u32 s43, 0x6a80
	s_cbranch_scc0 .Lcvb24_wait
	s_add_u32 s43, s32, 0
	s_cmp_lt_u32 s43, 0x600
	s_cbranch_scc0 .Lcvb24_d0_b
	s_mul_i32 s58, s43, 0xaaab
	s_lshr_b32 s58, s58, 22
	s_mul_i32 s59, s58, 96
	s_sub_u32 s59, s43, s59
	s_mul_i32 s60, s58, 0xc0000
	s_mul_i32 s81, s59, 0x80
	s_add_u32 s60, s60, s81
	s_add_u32 s92, s94, s60
	s_addc_u32 s93, s95, 0
	s_mov_b32 s63, 0x3000
	s_mul_i32 s61, s59, 0x8000
	s_mul_i32 s81, s58, 0x40
	s_add_u32 s61, s61, s81
	s_add_u32 s61, s61, 0x800000
	s_add_u32 s50, s48, s61
	s_addc_u32 s51, s49, 0
	s_mov_b32 s65, 0x400
	s_mov_b32 s71, 0x44000000
	s_branch .Lcvb24_d0_ld

.Lcvb24_skip:
	s_waitcnt lgkmcnt(0)
	s_barrier
.LBB0_2481:
	s_add_u32 s22, s90, 0x3000
	s_addc_u32 s23, s91, 0
	s_cmp_lt_i32 s84, 26
	s_cselect_b64 s[0:1], -1, 0
	s_cmp_gt_i32 s85, 25
	s_cselect_b64 s[2:3], -1, 0
	s_and_b64 s[0:1], s[0:1], s[2:3]
	s_andn2_b64 vcc, exec, s[0:1]
	s_cbranch_vccnz .LBB0_2551
	v_mbcnt_lo_u32_b32 v0, -1, 0
	v_readlane_b32 s0, v254, 5
	v_mbcnt_hi_u32_b32 v9, -1, v0
	s_andn2_b32 s0, s0, 63
	s_cmpk_gt_i32 s86, 0xff
	v_add_u32_e32 v50, s0, v9
	v_ashrrev_i32_e32 v51, 31, v50
	v_lshl_add_u64 v[42:43], v[50:51], 4, s[90:91]
	v_add_co_u32_e32 v0, vcc, 0x8300000, v42
	v_lshl_add_u32 v8, v50, 4, 0
	s_nop 0
	v_addc_co_u32_e32 v1, vcc, 0, v43, vcc
	v_add_co_u32_e32 v4, vcc, 0x8302000, v42
	v_add_u32_e32 v50, 0xa000, v8
	s_waitcnt lgkmcnt(0)
	v_addc_co_u32_e32 v5, vcc, 0, v43, vcc
	v_add_co_u32_e32 v10, vcc, 0x8304000, v42
	global_load_dwordx4 v[0:3], v[0:1], off
	s_nop 0
	global_load_dwordx4 v[4:7], v[4:5], off
	v_addc_co_u32_e32 v11, vcc, 0, v43, vcc
	v_add_co_u32_e32 v14, vcc, 0x8306000, v42
	v_add_u32_e32 v51, 0x1a000, v8
	s_nop 0
	v_addc_co_u32_e32 v15, vcc, 0, v43, vcc
	v_add_co_u32_e32 v18, vcc, 0x8308000, v42
	global_load_dwordx4 v[10:13], v[10:11], off
	s_nop 0
	global_load_dwordx4 v[14:17], v[14:15], off
	v_addc_co_u32_e32 v19, vcc, 0, v43, vcc
	v_add_co_u32_e32 v22, vcc, 0x830a000, v42
	v_add_u32_e32 v52, 0x1c000, v8
	s_nop 0
	v_addc_co_u32_e32 v23, vcc, 0, v43, vcc
	v_add_co_u32_e32 v26, vcc, 0x830c000, v42
	global_load_dwordx4 v[18:21], v[18:19], off
	s_nop 0
	global_load_dwordx4 v[22:25], v[22:23], off
	v_addc_co_u32_e32 v27, vcc, 0, v43, vcc
	v_add_co_u32_e32 v30, vcc, 0x830e000, v42
	v_add_u32_e32 v53, 0x1e000, v8
	s_nop 0
	v_addc_co_u32_e32 v31, vcc, 0, v43, vcc
	s_waitcnt vmcnt(0)
	v_add_co_u32_e32 v34, vcc, 0x8310000, v42
	global_load_dwordx4 v[26:29], v[26:27], off
	s_nop 0
	global_load_dwordx4 v[30:33], v[30:31], off
	v_addc_co_u32_e32 v35, vcc, 0, v43, vcc
	v_add_co_u32_e32 v38, vcc, 0x8312000, v42
	v_add_u32_e32 v54, 0x20000, v8
	s_nop 0
	v_addc_co_u32_e32 v39, vcc, 0, v43, vcc
	v_add_co_u32_e32 v44, vcc, 0x8314000, v42
	global_load_dwordx4 v[34:37], v[34:35], off
	s_nop 0
	global_load_dwordx4 v[38:41], v[38:39], off
	v_addc_co_u32_e32 v45, vcc, 0, v43, vcc
	v_add_co_u32_e32 v46, vcc, 0x8316000, v42
	s_nop 1
	v_addc_co_u32_e32 v47, vcc, 0, v43, vcc
	global_load_dwordx4 v[42:45], v[44:45], off
	s_nop 0
	global_load_dwordx4 v[46:49], v[46:47], off
	ds_write_b128 v8, v[0:3] offset:40960
	ds_write_b128 v8, v[4:7] offset:49152
	ds_write_b128 v8, v[10:13] offset:57344
	ds_write_b128 v50, v[14:17] offset:24576
	ds_write_b128 v50, v[18:21] offset:32768
	ds_write_b128 v50, v[22:25] offset:40960
	s_waitcnt vmcnt(5)
	ds_write_b128 v50, v[26:29] offset:49152
	s_waitcnt vmcnt(4)
	ds_write_b128 v50, v[30:33] offset:57344
	s_waitcnt vmcnt(3)
	ds_write_b128 v51, v[34:37]
	s_waitcnt vmcnt(2)
	ds_write_b128 v52, v[38:41]
	s_waitcnt vmcnt(1)
	ds_write_b128 v53, v[42:45]
	s_waitcnt vmcnt(0)
	ds_write_b128 v54, v[46:49]
	s_waitcnt lgkmcnt(0)
	s_barrier
	s_cbranch_scc1 .LBB0_2497
	v_readlane_b32 s5, v254, 41
	s_mul_i32 s0, s5, 0xd00
	s_lshl_b32 s30, s86, 3
	s_add_i32 s4, s0, 0
	v_readlane_b32 s0, v254, 5
	s_cmp_lt_u32 s0, 64
	v_ashrrev_i32_e32 v2, 4, v9
	v_cmp_gt_i32_e32 vcc, 32, v9
	s_cselect_b64 s[0:1], -1, 0
	v_lshl_add_u32 v8, v9, 2, 0
	v_lshlrev_b32_e32 v0, 3, v2
	s_and_b64 s[24:25], s[0:1], vcc
	v_ashrrev_i32_e32 v1, 31, v0
	v_mad_u64_u32 v[12:13], s[0:1], v9, 12, v[8:9]
	v_lshl_add_u64 v[10:11], v[0:1], 1, s[20:21]
	s_movk_i32 s0, 0xd0
	v_lshlrev_b32_e32 v0, 5, v9
	v_and_b32_e32 v16, 15, v9
	v_mul_lo_u32 v5, v9, s0
	v_ashrrev_i32_e32 v1, 31, v0
	s_movk_i32 s0, 0x340
	v_lshl_add_u32 v4, v16, 2, s4
	v_lshl_add_u64 v[14:15], v[0:1], 2, s[22:23]
	v_mul_lo_u32 v0, v2, s0
	s_lshl_b32 s0, s86, 7
	s_lshl_b32 s1, s5, 4
	v_add_u32_e32 v13, 0xa000, v12
	v_cmp_gt_i32_e64 s[2:3], 16, v9
	v_add_u32_e32 v17, 0x1a000, v12
	v_add_u32_e32 v18, 0x1a400, v12
	v_add_u32_e32 v19, 0x1a800, v12
	v_add_u32_e32 v20, 0x1ac00, v12
	v_add_u32_e32 v21, 0x1b000, v12
	v_add_u32_e32 v22, 0x1b400, v12
	v_add_u32_e32 v23, 0x1b800, v12
	v_add_u32_e32 v24, 0x1bc00, v12
	v_add_u32_e32 v25, 0x1c000, v12
	v_add_u32_e32 v26, 0x1c400, v12
	v_add_u32_e32 v27, 0x1c800, v12
	v_add_u32_e32 v28, 0x1cc00, v12
	v_add_u32_e32 v29, 0x1d000, v12
	v_add_u32_e32 v30, 0x1d400, v12
	v_add_u32_e32 v31, 0x1d800, v12
	v_add_u32_e32 v32, 0x1dc00, v12
	v_add_u32_e32 v33, 0x1e000, v12
	v_add_u32_e32 v34, 0x1e400, v12
	v_add_u32_e32 v35, 0x1e800, v12
	v_add_u32_e32 v36, 0x1ec00, v12
	v_add_u32_e32 v37, 0x1f000, v12
	v_add_u32_e32 v38, 0x1f400, v12
	v_add_u32_e32 v39, 0x1f800, v12
	v_add_u32_e32 v40, 0x1fc00, v12
	v_add_u32_e32 v41, 0x20000, v12
	v_add_u32_e32 v42, 0x20400, v12
	v_add_u32_e32 v43, 0x20800, v12
	v_add_u32_e32 v44, 0x20c00, v12
	v_add_u32_e32 v45, 0x21000, v12
	v_add_u32_e32 v46, 0x21400, v12
	v_add_u32_e32 v47, 0x21800, v12
	v_add_u32_e32 v48, 0x21c00, v12
	s_add_i32 s31, s0, s1
	s_lshl_b32 s33, s74, 7
	v_mov_b32_e32 v3, 0
	v_add_u32_e32 v49, v4, v0
	v_add_u32_e32 v50, s4, v5
	v_mov_b32_e32 v51, 1
	s_mov_b32 s34, 0xff800000
	v_mov_b32_e32 v52, 0xff800000
	s_branch .LBB0_2485

.LBB0_2550:
	s_or_b64 exec, exec, s[0:1]
	v_readlane_b32 s69, v254, 41
	s_nop 3
	s_cmp_eq_u32 s69, 0
	s_cbranch_scc1 .Lcvb25_skip
	s_waitcnt vmcnt(0) lgkmcnt(0)
	v_readlane_b32 s0, v254, 42
	v_readlane_b32 s1, v254, 43
	v_readlane_b32 s60, v254, 0
	v_readlane_b32 s61, v254, 41
	s_nop 3
	s_sub_u32 s0, s0, 0xd0
	s_subb_u32 s1, s1, 0
	s_load_dwordx2 s[94:95], s[0:1], 0x10
	s_load_dwordx2 s[98:99], s[0:1], 0x18
	s_load_dwordx2 s[56:57], s[0:1], 0x88
	s_load_dwordx2 s[82:83], s[0:1], 0x90
	s_load_dwordx2 s[38:39], s[0:1], 0x98
	s_load_dwordx2 s[44:45], s[0:1], 0xa0
	s_load_dwordx2 s[46:47], s[0:1], 0xa8
	s_load_dwordx2 s[48:49], s[0:1], 0xb8
	v_mbcnt_lo_u32_b32 v100, -1, 0
	v_mbcnt_hi_u32_b32 v100, -1, v100
	v_and_b32_e32 v96, 7, v100
	v_lshrrev_b32_e32 v97, 3, v100
	v_mov_b32_e32 v98, 0x43e00000
	s_mov_b32 s64, 0xc3e00000
	s_mul_i32 s32, s60, 7
	s_add_u32 s32, s32, s61
	s_sub_u32 s32, s32, 1
	s_mul_i32 s43, s74, 21
	s_add_u32 s32, s32, s43
	s_mul_i32 s32, s32, 3
	s_waitcnt lgkmcnt(0)
	s_add_u32 s94, s94, 0xc00000
	s_addc_u32 s95, s95, 0
	s_add_u32 s98, s98, 0x400000
	s_addc_u32 s99, s99, 0
	s_add_u32 s56, s56, 0xc000000
	s_addc_u32 s57, s57, 0
	s_add_u32 s82, s82, 0xc000000
	s_addc_u32 s83, s83, 0
	s_add_u32 s38, s38, 0xc000000
	s_addc_u32 s39, s39, 0
	s_add_u32 s44, s44, 0xc00000
	s_addc_u32 s45, s45, 0
	s_add_u32 s46, s46, 0x300000
	s_addc_u32 s47, s47, 0
	s_add_u32 s48, s48, 0x2bd00000
	s_addc_u32 s49, s49, 0
	s_mov_b32 s41, 0
	s_add_u32 s43, s32, 0
	s_cmp_lt_u32 s43, 0x6a80
	s_cbranch_scc0 .Lcvb25_wait
	s_add_u32 s43, s32, 0
	s_cmp_lt_u32 s43, 0x600
	s_cbranch_scc0 .Lcvb25_d0_b
	s_mul_i32 s58, s43, 0xaaab
	s_lshr_b32 s58, s58, 22
	s_mul_i32 s59, s58, 96
	s_sub_u32 s59, s43, s59
	s_mul_i32 s60, s58, 0xc0000
	s_mul_i32 s81, s59, 0x80
	s_add_u32 s60, s60, s81
	s_add_u32 s92, s94, s60
	s_addc_u32 s93, s95, 0
	s_mov_b32 s63, 0x3000
	s_mul_i32 s61, s59, 0x8000
	s_mul_i32 s81, s58, 0x40
	s_add_u32 s61, s61, s81
	s_add_u32 s61, s61, 0x800000
	s_add_u32 s50, s48, s61
	s_addc_u32 s51, s49, 0
	s_mov_b32 s65, 0x400
	s_mov_b32 s71, 0x44000000
	s_branch .Lcvb25_d0_ld

.Lcvb25_skip:
	s_waitcnt lgkmcnt(0)
	s_barrier
.LBB0_2551:
	s_cmp_gt_i32 s84, 26
	s_cselect_b64 s[6:7], -1, 0
	s_cmp_lt_i32 s84, 27
	s_cselect_b64 s[0:1], -1, 0
	s_cmp_gt_i32 s85, 26
	s_cselect_b64 s[2:3], -1, 0
	s_and_b64 s[0:1], s[0:1], s[2:3]
	s_andn2_b64 vcc, exec, s[0:1]
	s_cbranch_vccnz .LBB0_2649
	v_mbcnt_lo_u32_b32 v0, -1, 0
	v_mbcnt_hi_u32_b32 v1, -1, v0
	v_readlane_b32 s0, v254, 5
	v_mov_b32_e32 v4, v1
	s_and_b32 s33, s0, 0xffffffc0
	s_waitcnt vmcnt(0) lgkmcnt(0)
	v_add_u32_e32 v0, s33, v4
	v_cmp_gt_i32_e32 vcc, 64, v0
	s_barrier
	s_and_saveexec_b64 s[2:3], vcc
	s_cbranch_execz .LBB0_2558
	v_cmp_gt_i32_e32 vcc, 32, v0
	v_mov_b32_e32 v2, 0
	s_and_saveexec_b64 s[0:1], vcc
	s_cbranch_execz .LBB0_2555
	v_lshlrev_b32_e32 v2, 5, v0
	v_ashrrev_i32_e32 v3, 31, v2
	v_lshl_add_u64 v[2:3], v[2:3], 2, s[22:23]
	global_load_dword v2, v[2:3], off

.LBB0_2648:
	s_or_b64 exec, exec, s[0:1]
	v_readlane_b32 s69, v254, 41
	s_nop 3
	s_cmp_eq_u32 s69, 0
	s_cbranch_scc1 .Lcvb26_skip
	s_waitcnt vmcnt(0) lgkmcnt(0)
	v_readlane_b32 s0, v254, 42
	v_readlane_b32 s1, v254, 43
	v_readlane_b32 s60, v254, 0
	v_readlane_b32 s61, v254, 41
	s_nop 3
	s_sub_u32 s0, s0, 0xd0
	s_subb_u32 s1, s1, 0
	s_load_dwordx2 s[94:95], s[0:1], 0x10
	s_load_dwordx2 s[98:99], s[0:1], 0x18
	s_load_dwordx2 s[56:57], s[0:1], 0x88
	s_load_dwordx2 s[82:83], s[0:1], 0x90
	s_load_dwordx2 s[38:39], s[0:1], 0x98
	s_load_dwordx2 s[44:45], s[0:1], 0xa0
	s_load_dwordx2 s[46:47], s[0:1], 0xa8
	s_load_dwordx2 s[48:49], s[0:1], 0xb8
	v_mbcnt_lo_u32_b32 v100, -1, 0
	v_mbcnt_hi_u32_b32 v100, -1, v100
	v_and_b32_e32 v96, 7, v100
	v_lshrrev_b32_e32 v97, 3, v100
	v_mov_b32_e32 v98, 0x43e00000
	s_mov_b32 s64, 0xc3e00000
	s_mul_i32 s32, s60, 7
	s_add_u32 s32, s32, s61
	s_sub_u32 s32, s32, 1
	s_mul_i32 s43, s74, 28
	s_add_u32 s32, s32, s43
	s_mul_i32 s32, s32, 3
	s_waitcnt lgkmcnt(0)
	s_add_u32 s94, s94, 0xc00000
	s_addc_u32 s95, s95, 0
	s_add_u32 s98, s98, 0x400000
	s_addc_u32 s99, s99, 0
	s_add_u32 s56, s56, 0xc000000
	s_addc_u32 s57, s57, 0
	s_add_u32 s82, s82, 0xc000000
	s_addc_u32 s83, s83, 0
	s_add_u32 s38, s38, 0xc000000
	s_addc_u32 s39, s39, 0
	s_add_u32 s44, s44, 0xc00000
	s_addc_u32 s45, s45, 0
	s_add_u32 s46, s46, 0x300000
	s_addc_u32 s47, s47, 0
	s_add_u32 s48, s48, 0x2bd00000
	s_addc_u32 s49, s49, 0
	s_mov_b32 s41, 0
	s_add_u32 s43, s32, 0
	s_cmp_lt_u32 s43, 0x6a80
	s_cbranch_scc0 .Lcvb26_wait
	s_add_u32 s43, s32, 0
	s_cmp_lt_u32 s43, 0x600
	s_cbranch_scc0 .Lcvb26_d0_b
	s_mul_i32 s58, s43, 0xaaab
	s_lshr_b32 s58, s58, 22
	s_mul_i32 s59, s58, 96
	s_sub_u32 s59, s43, s59
	s_mul_i32 s60, s58, 0xc0000
	s_mul_i32 s81, s59, 0x80
	s_add_u32 s60, s60, s81
	s_add_u32 s92, s94, s60
	s_addc_u32 s93, s95, 0
	s_mov_b32 s63, 0x3000
	s_mul_i32 s61, s59, 0x8000
	s_mul_i32 s81, s58, 0x40
	s_add_u32 s61, s61, s81
	s_add_u32 s61, s61, 0x800000
	s_add_u32 s50, s48, s61
	s_addc_u32 s51, s49, 0
	s_mov_b32 s65, 0x400
	s_mov_b32 s71, 0x44000000
	s_branch .Lcvb26_d0_ld

.Lcvb26_skip:
	s_waitcnt lgkmcnt(0)
	s_barrier
.LBB0_2649:
	s_cmp_lt_i32 s84, 28
	s_cselect_b64 s[0:1], -1, 0
	s_cmp_gt_i32 s85, 27
	s_cselect_b64 s[2:3], -1, 0
	s_and_b64 s[0:1], s[0:1], s[2:3]
	v_cndmask_b32_e64 v0, 0, 1, s[6:7]
	s_andn2_b64 vcc, exec, s[0:1]
	v_cmp_ne_u32_e64 s[2:3], 1, v0
	s_cbranch_vccnz .LBB0_2739
	s_and_b64 vcc, exec, s[2:3]
	s_cbranch_vccnz .LBB0_2658
	v_mbcnt_lo_u32_b32 v0, -1, 0
	v_mbcnt_hi_u32_b32 v1, -1, v0
	v_readlane_b32 s0, v254, 5
	v_mov_b32_e32 v4, v1
	s_andn2_b32 s0, s0, 63
	s_waitcnt vmcnt(0) lgkmcnt(0)
	v_add_u32_e32 v0, s0, v4
	v_cmp_gt_i32_e32 vcc, 64, v0
	s_barrier
	s_and_saveexec_b64 s[4:5], vcc
	s_cbranch_execz .LBB0_2657
	v_cmp_gt_i32_e32 vcc, 32, v0
	v_mov_b32_e32 v2, 0
	s_and_saveexec_b64 s[0:1], vcc
	s_cbranch_execz .LBB0_2654
	v_lshlrev_b32_e32 v2, 5, v0
	v_ashrrev_i32_e32 v3, 31, v2
	v_lshl_add_u64 v[2:3], v[2:3], 2, s[22:23]
	global_load_dword v2, v[2:3], off

.LBB0_2738:
	s_or_b64 exec, exec, s[0:1]
	v_readlane_b32 s69, v254, 41
	s_nop 3
	s_cmp_eq_u32 s69, 0
	s_cbranch_scc1 .Lcvb27_skip
	s_waitcnt vmcnt(0) lgkmcnt(0)
	v_readlane_b32 s0, v254, 42
	v_readlane_b32 s1, v254, 43
	v_readlane_b32 s60, v254, 0
	v_readlane_b32 s61, v254, 41
	s_nop 3
	s_sub_u32 s0, s0, 0xd0
	s_subb_u32 s1, s1, 0
	s_load_dwordx2 s[94:95], s[0:1], 0x10
	s_load_dwordx2 s[98:99], s[0:1], 0x18
	s_load_dwordx2 s[56:57], s[0:1], 0x88
	s_load_dwordx2 s[82:83], s[0:1], 0x90
	s_load_dwordx2 s[38:39], s[0:1], 0x98
	s_load_dwordx2 s[44:45], s[0:1], 0xa0
	s_load_dwordx2 s[46:47], s[0:1], 0xa8
	s_load_dwordx2 s[48:49], s[0:1], 0xb8
	v_mbcnt_lo_u32_b32 v100, -1, 0
	v_mbcnt_hi_u32_b32 v100, -1, v100
	v_and_b32_e32 v96, 7, v100
	v_lshrrev_b32_e32 v97, 3, v100
	v_mov_b32_e32 v98, 0x43e00000
	s_mov_b32 s64, 0xc3e00000
	s_mul_i32 s32, s60, 7
	s_add_u32 s32, s32, s61
	s_sub_u32 s32, s32, 1
	s_mul_i32 s43, s74, 35
	s_add_u32 s32, s32, s43
	s_mul_i32 s32, s32, 3
	s_waitcnt lgkmcnt(0)
	s_add_u32 s94, s94, 0xc00000
	s_addc_u32 s95, s95, 0
	s_add_u32 s98, s98, 0x400000
	s_addc_u32 s99, s99, 0
	s_add_u32 s56, s56, 0xc000000
	s_addc_u32 s57, s57, 0
	s_add_u32 s82, s82, 0xc000000
	s_addc_u32 s83, s83, 0
	s_add_u32 s38, s38, 0xc000000
	s_addc_u32 s39, s39, 0
	s_add_u32 s44, s44, 0xc00000
	s_addc_u32 s45, s45, 0
	s_add_u32 s46, s46, 0x300000
	s_addc_u32 s47, s47, 0
	s_add_u32 s48, s48, 0x2bd00000
	s_addc_u32 s49, s49, 0
	s_mov_b32 s41, 0
	s_add_u32 s43, s32, 0
	s_cmp_lt_u32 s43, 0x6a80
	s_cbranch_scc0 .Lcvb27_wait
	s_add_u32 s43, s32, 0
	s_cmp_lt_u32 s43, 0x600
	s_cbranch_scc0 .Lcvb27_d0_b
	s_mul_i32 s58, s43, 0xaaab
	s_lshr_b32 s58, s58, 22
	s_mul_i32 s59, s58, 96
	s_sub_u32 s59, s43, s59
	s_mul_i32 s60, s58, 0xc0000
	s_mul_i32 s81, s59, 0x80
	s_add_u32 s60, s60, s81
	s_add_u32 s92, s94, s60
	s_addc_u32 s93, s95, 0
	s_mov_b32 s63, 0x3000
	s_mul_i32 s61, s59, 0x8000
	s_mul_i32 s81, s58, 0x40
	s_add_u32 s61, s61, s81
	s_add_u32 s61, s61, 0x800000
	s_add_u32 s50, s48, s61
	s_addc_u32 s51, s49, 0
	s_mov_b32 s65, 0x400
	s_mov_b32 s71, 0x44000000
	s_branch .Lcvb27_d0_ld

.Lcvb27_skip:
	s_waitcnt lgkmcnt(0)
	s_barrier
.LBB0_2739:
	s_cmp_lt_i32 s84, 29
	s_cselect_b64 s[0:1], -1, 0
	s_cmp_gt_i32 s85, 28
	s_cselect_b64 s[4:5], -1, 0
	s_and_b64 s[0:1], s[0:1], s[4:5]
	s_andn2_b64 vcc, exec, s[0:1]
	s_cbranch_vccnz .LBB0_2805
	v_mbcnt_lo_u32_b32 v0, -1, 0
	s_waitcnt vmcnt(0)
	v_mbcnt_hi_u32_b32 v32, -1, v0
	v_mov_b32_e32 v0, v32
	s_and_b64 vcc, exec, s[2:3]
	s_cbranch_vccnz .LBB0_2748
	v_readlane_b32 s0, v254, 5
	s_andn2_b32 s0, s0, 63
	s_waitcnt lgkmcnt(0)
	v_add_u32_e32 v1, s0, v0
	v_cmp_gt_i32_e32 vcc, 64, v1
	s_barrier
	s_and_saveexec_b64 s[4:5], vcc
	s_cbranch_execz .LBB0_2747
	v_cmp_gt_i32_e32 vcc, 32, v1
	v_mov_b32_e32 v2, 0
	s_and_saveexec_b64 s[0:1], vcc
	s_cbranch_execz .LBB0_2744
	v_lshlrev_b32_e32 v2, 5, v1
	v_ashrrev_i32_e32 v3, 31, v2
	v_lshl_add_u64 v[2:3], v[2:3], 2, s[22:23]
	global_load_dword v2, v[2:3], off
